# P8 router K loop hand-written: 16-byte residual-row loads (lane takes 8 consecutive k), operands two chunks ahead in three register buffers, same exact-f32 32x32x2 MFMAs
# speedup vs baseline: 1.0046x; 1.0046x over previous
; __device__ __forceinline__ float bf_lo(unsigned w) { return __uint_as_float(w << 16); }
; __device__ __forceinline__ float bf_hi(unsigned w) { return __uint_as_float(w & 0xffff0000u); }
; __global__ void __launch_bounds__(512, 2) fwd_kernel(Params p) {
;     ...
;                 const bf16_t* xr = X1 + (size_t)(blk * 64 + tt * 32 + j) * DM + kq * 512 + hh * 4;
;                 const float* wr_ = WrT + (size_t)j * DM + kq * 512 + hh * 4;
;                 f32x16 acc = {}; float ss = 0.f;
;                 u32x2 xb[2][8]; f32x4 wb[2][8];
; #pragma unroll
;                 for (int i = 0; i < 8; ++i) { xb[0][i] = *(const u32x2*)(xr + i * 8); wb[0][i] = *(const f32x4*)(wr_ + i * 8); }
; #pragma unroll
;                 for (int ch = 0; ch < 8; ++ch) {
;                     if (ch + 1 < 8) {
; #pragma unroll
;                         for (int i = 0; i < 8; ++i) { xb[(ch + 1) & 1][i] = *(const u32x2*)(xr + (ch + 1) * 64 + i * 8); wb[(ch + 1) & 1][i] = *(const f32x4*)(wr_ + (ch + 1) * 64 + i * 8); } }
; #pragma unroll
;                     for (int i = 0; i < 8; ++i) { const u32x2 xp = xb[ch & 1][i]; const f32x4 xv = {bf_lo(xp.x), bf_hi(xp.x), bf_lo(xp.y), bf_hi(xp.y)}, wv = wb[ch & 1][i];
;                         acc = __builtin_amdgcn_mfma_f32_32x32x2f32(wv.x, xv.x, acc, 0, 0, 0); acc = __builtin_amdgcn_mfma_f32_32x32x2f32(wv.y, xv.y, acc, 0, 0, 0);
;                         acc = __builtin_amdgcn_mfma_f32_32x32x2f32(wv.z, xv.z, acc, 0, 0, 0); acc = __builtin_amdgcn_mfma_f32_32x32x2f32(wv.w, xv.w, acc, 0, 0, 0);
;                         ss += (xv.x * xv.x + xv.y * xv.y) + (xv.z * xv.z + xv.w * xv.w); }
;                 }
.LBB0_982:
	s_and_saveexec_b64 s[10:11], s[4:5]
	ds_write_b32 v132, v87 offset:53760
	s_or_b64 exec, exec, s[10:11]
	s_lshl_b32 s10, s78, 6
	v_or_b32_e32 v0, s10, v133
	v_ashrrev_i32_e32 v1, 31, v0
	v_lshlrev_b64 v[0:1], 12, v[0:1]
	v_lshl_add_u64 v[98:99], v[88:89], 0, v[0:1]
	v_mbcnt_lo_u32_b32 v81, -1, 0
	v_mbcnt_hi_u32_b32 v81, -1, v81
	v_lshrrev_b32_e32 v81, 5, v81
	v_mov_b32_e32 v83, 0
	v_lshlrev_b32_e32 v82, 3, v81
	v_lshl_add_u64 v[100:101], v[98:99], 0, v[82:83]
	v_lshlrev_b32_e32 v82, 4, v81
	v_lshl_add_u64 v[102:103], v[90:91], 0, v[82:83]
	v_mov_b32_e32 v80, 0
	global_load_dwordx4 v[148:151], v[100:101], off
	global_load_dwordx4 v[152:155], v[102:103], off
	global_load_dwordx4 v[156:159], v[102:103], off offset:16
	global_load_dwordx4 v[160:163], v[100:101], off offset:32
	global_load_dwordx4 v[164:167], v[102:103], off offset:64
	global_load_dwordx4 v[168:171], v[102:103], off offset:80
	global_load_dwordx4 v[172:175], v[100:101], off offset:64
	global_load_dwordx4 v[176:179], v[102:103], off offset:128
	global_load_dwordx4 v[180:183], v[102:103], off offset:144
	global_load_dwordx4 v[184:187], v[100:101], off offset:96
	global_load_dwordx4 v[188:191], v[102:103], off offset:192
	global_load_dwordx4 v[192:195], v[102:103], off offset:208
	global_load_dwordx4 v[196:199], v[100:101], off offset:128
	global_load_dwordx4 v[200:203], v[102:103], off offset:256
	global_load_dwordx4 v[204:207], v[102:103], off offset:272
	global_load_dwordx4 v[208:211], v[100:101], off offset:160
	global_load_dwordx4 v[212:215], v[102:103], off offset:320
	global_load_dwordx4 v[216:219], v[102:103], off offset:336
	global_load_dwordx4 v[220:223], v[100:101], off offset:192
	global_load_dwordx4 v[224:227], v[102:103], off offset:384
	global_load_dwordx4 v[228:231], v[102:103], off offset:400
	global_load_dwordx4 v[232:235], v[100:101], off offset:224
	global_load_dwordx4 v[236:239], v[102:103], off offset:448
	global_load_dwordx4 v[240:243], v[102:103], off offset:464
	global_load_dwordx4 v[16:19], v[100:101], off offset:256
	global_load_dwordx4 v[20:23], v[102:103], off offset:512
	global_load_dwordx4 v[24:27], v[102:103], off offset:528
	global_load_dwordx4 v[28:31], v[100:101], off offset:288
	global_load_dwordx4 v[32:35], v[102:103], off offset:576
	global_load_dwordx4 v[36:39], v[102:103], off offset:592
	global_load_dwordx4 v[40:43], v[100:101], off offset:320
	global_load_dwordx4 v[44:47], v[102:103], off offset:640
	global_load_dwordx4 v[48:51], v[102:103], off offset:656
	global_load_dwordx4 v[52:55], v[100:101], off offset:352
	global_load_dwordx4 v[56:59], v[102:103], off offset:704
	global_load_dwordx4 v[60:63], v[102:103], off offset:720
	s_waitcnt vmcnt(33)
	v_lshlrev_b32_e32 v64, 16, v148
	v_and_b32_e32 v65, 0xffff0000, v148
	v_lshlrev_b32_e32 v66, 16, v149
	v_and_b32_e32 v67, 0xffff0000, v149
	v_lshlrev_b32_e32 v68, 16, v150
	v_and_b32_e32 v69, 0xffff0000, v150
	v_lshlrev_b32_e32 v70, 16, v151
	v_and_b32_e32 v71, 0xffff0000, v151
	s_waitcnt vmcnt(30)
	v_mfma_f32_32x32x2_f32 v[0:15], v152, v64, 0
	v_lshlrev_b32_e32 v72, 16, v160
	v_fmac_f32_e32 v80, v64, v64
	v_mfma_f32_32x32x2_f32 v[0:15], v153, v65, v[0:15]
	v_and_b32_e32 v73, 0xffff0000, v160
	v_fmac_f32_e32 v80, v65, v65
	v_mfma_f32_32x32x2_f32 v[0:15], v154, v66, v[0:15]
	v_lshlrev_b32_e32 v74, 16, v161
	v_fmac_f32_e32 v80, v66, v66
	v_mfma_f32_32x32x2_f32 v[0:15], v155, v67, v[0:15]
	v_and_b32_e32 v75, 0xffff0000, v161
	v_fmac_f32_e32 v80, v67, v67
	v_mfma_f32_32x32x2_f32 v[0:15], v156, v68, v[0:15]
	v_lshlrev_b32_e32 v76, 16, v162
	v_fmac_f32_e32 v80, v68, v68
	v_mfma_f32_32x32x2_f32 v[0:15], v157, v69, v[0:15]
	v_and_b32_e32 v77, 0xffff0000, v162
	v_fmac_f32_e32 v80, v69, v69
	v_mfma_f32_32x32x2_f32 v[0:15], v158, v70, v[0:15]
	v_lshlrev_b32_e32 v78, 16, v163
	v_fmac_f32_e32 v80, v70, v70
	v_mfma_f32_32x32x2_f32 v[0:15], v159, v71, v[0:15]
	v_and_b32_e32 v79, 0xffff0000, v163
	v_fmac_f32_e32 v80, v71, v71
	s_waitcnt vmcnt(27)
	v_mfma_f32_32x32x2_f32 v[0:15], v164, v72, v[0:15]
	v_lshlrev_b32_e32 v64, 16, v172
	v_fmac_f32_e32 v80, v72, v72
	v_mfma_f32_32x32x2_f32 v[0:15], v165, v73, v[0:15]
	v_and_b32_e32 v65, 0xffff0000, v172
	v_fmac_f32_e32 v80, v73, v73
	v_mfma_f32_32x32x2_f32 v[0:15], v166, v74, v[0:15]
	v_lshlrev_b32_e32 v66, 16, v173
	v_fmac_f32_e32 v80, v74, v74
	v_mfma_f32_32x32x2_f32 v[0:15], v167, v75, v[0:15]
	v_and_b32_e32 v67, 0xffff0000, v173
	v_fmac_f32_e32 v80, v75, v75
	v_mfma_f32_32x32x2_f32 v[0:15], v168, v76, v[0:15]
	v_lshlrev_b32_e32 v68, 16, v174
	v_fmac_f32_e32 v80, v76, v76
	v_mfma_f32_32x32x2_f32 v[0:15], v169, v77, v[0:15]
	v_and_b32_e32 v69, 0xffff0000, v174
	v_fmac_f32_e32 v80, v77, v77
	v_mfma_f32_32x32x2_f32 v[0:15], v170, v78, v[0:15]
	v_lshlrev_b32_e32 v70, 16, v175
	v_fmac_f32_e32 v80, v78, v78
	v_mfma_f32_32x32x2_f32 v[0:15], v171, v79, v[0:15]
	v_and_b32_e32 v71, 0xffff0000, v175
	v_fmac_f32_e32 v80, v79, v79
	s_waitcnt vmcnt(24)
	v_mfma_f32_32x32x2_f32 v[0:15], v176, v64, v[0:15]
	v_lshlrev_b32_e32 v72, 16, v184
	v_fmac_f32_e32 v80, v64, v64
	v_mfma_f32_32x32x2_f32 v[0:15], v177, v65, v[0:15]
	v_and_b32_e32 v73, 0xffff0000, v184
	v_fmac_f32_e32 v80, v65, v65
	v_mfma_f32_32x32x2_f32 v[0:15], v178, v66, v[0:15]
	v_lshlrev_b32_e32 v74, 16, v185
	v_fmac_f32_e32 v80, v66, v66
	v_mfma_f32_32x32x2_f32 v[0:15], v179, v67, v[0:15]
	v_and_b32_e32 v75, 0xffff0000, v185
	v_fmac_f32_e32 v80, v67, v67
	v_mfma_f32_32x32x2_f32 v[0:15], v180, v68, v[0:15]
	v_lshlrev_b32_e32 v76, 16, v186
	v_fmac_f32_e32 v80, v68, v68
	v_mfma_f32_32x32x2_f32 v[0:15], v181, v69, v[0:15]
	v_and_b32_e32 v77, 0xffff0000, v186
	v_fmac_f32_e32 v80, v69, v69
	v_mfma_f32_32x32x2_f32 v[0:15], v182, v70, v[0:15]
	v_lshlrev_b32_e32 v78, 16, v187
	v_fmac_f32_e32 v80, v70, v70
	v_mfma_f32_32x32x2_f32 v[0:15], v183, v71, v[0:15]
	v_and_b32_e32 v79, 0xffff0000, v187
	v_fmac_f32_e32 v80, v71, v71
	s_waitcnt vmcnt(21)
; __device__ __forceinline__ float bf_lo(unsigned w) { return __uint_as_float(w << 16); }
; __device__ __forceinline__ float bf_hi(unsigned w) { return __uint_as_float(w & 0xffff0000u); }
; __global__ void __launch_bounds__(512, 2) fwd_kernel(Params p) {
;     ...
;                 const bf16_t* xr = X1 + (size_t)(blk * 64 + tt * 32 + j) * DM + kq * 512 + hh * 4;
;                 const float* wr_ = WrT + (size_t)j * DM + kq * 512 + hh * 4;
;                 f32x16 acc = {}; float ss = 0.f;
;                 u32x2 xb[2][8]; f32x4 wb[2][8];
; #pragma unroll
;                 for (int i = 0; i < 8; ++i) { xb[0][i] = *(const u32x2*)(xr + i * 8); wb[0][i] = *(const f32x4*)(wr_ + i * 8); }
; #pragma unroll
;                 for (int ch = 0; ch < 8; ++ch) {
;                     if (ch + 1 < 8) {
; #pragma unroll
;                         for (int i = 0; i < 8; ++i) { xb[(ch + 1) & 1][i] = *(const u32x2*)(xr + (ch + 1) * 64 + i * 8); wb[(ch + 1) & 1][i] = *(const f32x4*)(wr_ + (ch + 1) * 64 + i * 8); } }
; #pragma unroll
;                     for (int i = 0; i < 8; ++i) { const u32x2 xp = xb[ch & 1][i]; const f32x4 xv = {bf_lo(xp.x), bf_hi(xp.x), bf_lo(xp.y), bf_hi(xp.y)}, wv = wb[ch & 1][i];
;                         acc = __builtin_amdgcn_mfma_f32_32x32x2f32(wv.x, xv.x, acc, 0, 0, 0); acc = __builtin_amdgcn_mfma_f32_32x32x2f32(wv.y, xv.y, acc, 0, 0, 0);
;                         acc = __builtin_amdgcn_mfma_f32_32x32x2f32(wv.z, xv.z, acc, 0, 0, 0); acc = __builtin_amdgcn_mfma_f32_32x32x2f32(wv.w, xv.w, acc, 0, 0, 0);
;                         ss += (xv.x * xv.x + xv.y * xv.y) + (xv.z * xv.z + xv.w * xv.w); }
;                 }
	v_mfma_f32_32x32x2_f32 v[0:15], v188, v72, v[0:15]
	v_lshlrev_b32_e32 v64, 16, v196
	v_fmac_f32_e32 v80, v72, v72
	v_mfma_f32_32x32x2_f32 v[0:15], v189, v73, v[0:15]
	v_and_b32_e32 v65, 0xffff0000, v196
	v_fmac_f32_e32 v80, v73, v73
	v_mfma_f32_32x32x2_f32 v[0:15], v190, v74, v[0:15]
	v_lshlrev_b32_e32 v66, 16, v197
	v_fmac_f32_e32 v80, v74, v74
	v_mfma_f32_32x32x2_f32 v[0:15], v191, v75, v[0:15]
	v_and_b32_e32 v67, 0xffff0000, v197
	v_fmac_f32_e32 v80, v75, v75
	v_mfma_f32_32x32x2_f32 v[0:15], v192, v76, v[0:15]
	v_lshlrev_b32_e32 v68, 16, v198
	v_fmac_f32_e32 v80, v76, v76
	v_mfma_f32_32x32x2_f32 v[0:15], v193, v77, v[0:15]
	v_and_b32_e32 v69, 0xffff0000, v198
	v_fmac_f32_e32 v80, v77, v77
	v_mfma_f32_32x32x2_f32 v[0:15], v194, v78, v[0:15]
	v_lshlrev_b32_e32 v70, 16, v199
	v_fmac_f32_e32 v80, v78, v78
	v_mfma_f32_32x32x2_f32 v[0:15], v195, v79, v[0:15]
	v_and_b32_e32 v71, 0xffff0000, v199
	v_fmac_f32_e32 v80, v79, v79
	global_load_dwordx4 v[148:151], v[100:101], off offset:384
	global_load_dwordx4 v[152:155], v[102:103], off offset:768
	global_load_dwordx4 v[156:159], v[102:103], off offset:784
	global_load_dwordx4 v[160:163], v[100:101], off offset:416
	global_load_dwordx4 v[164:167], v[102:103], off offset:832
	global_load_dwordx4 v[168:171], v[102:103], off offset:848
	global_load_dwordx4 v[172:175], v[100:101], off offset:448
	global_load_dwordx4 v[176:179], v[102:103], off offset:896
	global_load_dwordx4 v[180:183], v[102:103], off offset:912
	global_load_dwordx4 v[184:187], v[100:101], off offset:480
	global_load_dwordx4 v[188:191], v[102:103], off offset:960
	global_load_dwordx4 v[192:195], v[102:103], off offset:976
	s_waitcnt vmcnt(30)
	v_mfma_f32_32x32x2_f32 v[0:15], v200, v64, v[0:15]
	v_lshlrev_b32_e32 v72, 16, v208
	v_fmac_f32_e32 v80, v64, v64
	v_mfma_f32_32x32x2_f32 v[0:15], v201, v65, v[0:15]
	v_and_b32_e32 v73, 0xffff0000, v208
	v_fmac_f32_e32 v80, v65, v65
	v_mfma_f32_32x32x2_f32 v[0:15], v202, v66, v[0:15]
	v_lshlrev_b32_e32 v74, 16, v209
	v_fmac_f32_e32 v80, v66, v66
	v_mfma_f32_32x32x2_f32 v[0:15], v203, v67, v[0:15]
	v_and_b32_e32 v75, 0xffff0000, v209
	v_fmac_f32_e32 v80, v67, v67
	v_mfma_f32_32x32x2_f32 v[0:15], v204, v68, v[0:15]
	v_lshlrev_b32_e32 v76, 16, v210
	v_fmac_f32_e32 v80, v68, v68
	v_mfma_f32_32x32x2_f32 v[0:15], v205, v69, v[0:15]
	v_and_b32_e32 v77, 0xffff0000, v210
	v_fmac_f32_e32 v80, v69, v69
	v_mfma_f32_32x32x2_f32 v[0:15], v206, v70, v[0:15]
	v_lshlrev_b32_e32 v78, 16, v211
	v_fmac_f32_e32 v80, v70, v70
	v_mfma_f32_32x32x2_f32 v[0:15], v207, v71, v[0:15]
	v_and_b32_e32 v79, 0xffff0000, v211
	v_fmac_f32_e32 v80, v71, v71
	s_waitcnt vmcnt(27)
	v_mfma_f32_32x32x2_f32 v[0:15], v212, v72, v[0:15]
	v_lshlrev_b32_e32 v64, 16, v220
	v_fmac_f32_e32 v80, v72, v72
	v_mfma_f32_32x32x2_f32 v[0:15], v213, v73, v[0:15]
	v_and_b32_e32 v65, 0xffff0000, v220
	v_fmac_f32_e32 v80, v73, v73
	v_mfma_f32_32x32x2_f32 v[0:15], v214, v74, v[0:15]
	v_lshlrev_b32_e32 v66, 16, v221
	v_fmac_f32_e32 v80, v74, v74
	v_mfma_f32_32x32x2_f32 v[0:15], v215, v75, v[0:15]
	v_and_b32_e32 v67, 0xffff0000, v221
	v_fmac_f32_e32 v80, v75, v75
	v_mfma_f32_32x32x2_f32 v[0:15], v216, v76, v[0:15]
	v_lshlrev_b32_e32 v68, 16, v222
	v_fmac_f32_e32 v80, v76, v76
	v_mfma_f32_32x32x2_f32 v[0:15], v217, v77, v[0:15]
	v_and_b32_e32 v69, 0xffff0000, v222
	v_fmac_f32_e32 v80, v77, v77
	v_mfma_f32_32x32x2_f32 v[0:15], v218, v78, v[0:15]
	v_lshlrev_b32_e32 v70, 16, v223
	v_fmac_f32_e32 v80, v78, v78
	v_mfma_f32_32x32x2_f32 v[0:15], v219, v79, v[0:15]
	v_and_b32_e32 v71, 0xffff0000, v223
	v_fmac_f32_e32 v80, v79, v79
	s_waitcnt vmcnt(24)
	v_mfma_f32_32x32x2_f32 v[0:15], v224, v64, v[0:15]
	v_lshlrev_b32_e32 v72, 16, v232
	v_fmac_f32_e32 v80, v64, v64
	v_mfma_f32_32x32x2_f32 v[0:15], v225, v65, v[0:15]
	v_and_b32_e32 v73, 0xffff0000, v232
	v_fmac_f32_e32 v80, v65, v65
	v_mfma_f32_32x32x2_f32 v[0:15], v226, v66, v[0:15]
	v_lshlrev_b32_e32 v74, 16, v233
	v_fmac_f32_e32 v80, v66, v66
	v_mfma_f32_32x32x2_f32 v[0:15], v227, v67, v[0:15]
	v_and_b32_e32 v75, 0xffff0000, v233
	v_fmac_f32_e32 v80, v67, v67
	v_mfma_f32_32x32x2_f32 v[0:15], v228, v68, v[0:15]
	v_lshlrev_b32_e32 v76, 16, v234
	v_fmac_f32_e32 v80, v68, v68
	v_mfma_f32_32x32x2_f32 v[0:15], v229, v69, v[0:15]
	v_and_b32_e32 v77, 0xffff0000, v234
	v_fmac_f32_e32 v80, v69, v69
	v_mfma_f32_32x32x2_f32 v[0:15], v230, v70, v[0:15]
	v_lshlrev_b32_e32 v78, 16, v235
	v_fmac_f32_e32 v80, v70, v70
	v_mfma_f32_32x32x2_f32 v[0:15], v231, v71, v[0:15]
	v_and_b32_e32 v79, 0xffff0000, v235
	v_fmac_f32_e32 v80, v71, v71
	s_waitcnt vmcnt(21)
	v_mfma_f32_32x32x2_f32 v[0:15], v236, v72, v[0:15]
	v_lshlrev_b32_e32 v64, 16, v16
	v_fmac_f32_e32 v80, v72, v72
	v_mfma_f32_32x32x2_f32 v[0:15], v237, v73, v[0:15]
	v_and_b32_e32 v65, 0xffff0000, v16
	v_fmac_f32_e32 v80, v73, v73
	v_mfma_f32_32x32x2_f32 v[0:15], v238, v74, v[0:15]
	v_lshlrev_b32_e32 v66, 16, v17
	v_fmac_f32_e32 v80, v74, v74
	v_mfma_f32_32x32x2_f32 v[0:15], v239, v75, v[0:15]
	v_and_b32_e32 v67, 0xffff0000, v17
	v_fmac_f32_e32 v80, v75, v75
	v_mfma_f32_32x32x2_f32 v[0:15], v240, v76, v[0:15]
	v_lshlrev_b32_e32 v68, 16, v18
	v_fmac_f32_e32 v80, v76, v76
	v_mfma_f32_32x32x2_f32 v[0:15], v241, v77, v[0:15]
	v_and_b32_e32 v69, 0xffff0000, v18
	v_fmac_f32_e32 v80, v77, v77
	v_mfma_f32_32x32x2_f32 v[0:15], v242, v78, v[0:15]
	v_lshlrev_b32_e32 v70, 16, v19
	v_fmac_f32_e32 v80, v78, v78
	v_mfma_f32_32x32x2_f32 v[0:15], v243, v79, v[0:15]
	v_and_b32_e32 v71, 0xffff0000, v19
	v_fmac_f32_e32 v80, v79, v79
	global_load_dwordx4 v[196:199], v[100:101], off offset:512
	global_load_dwordx4 v[200:203], v[102:103], off offset:1024
	global_load_dwordx4 v[204:207], v[102:103], off offset:1040
	global_load_dwordx4 v[208:211], v[100:101], off offset:544
	global_load_dwordx4 v[212:215], v[102:103], off offset:1088
	global_load_dwordx4 v[216:219], v[102:103], off offset:1104
	global_load_dwordx4 v[220:223], v[100:101], off offset:576
	global_load_dwordx4 v[224:227], v[102:103], off offset:1152
	global_load_dwordx4 v[228:231], v[102:103], off offset:1168
	global_load_dwordx4 v[232:235], v[100:101], off offset:608
	global_load_dwordx4 v[236:239], v[102:103], off offset:1216
	global_load_dwordx4 v[240:243], v[102:103], off offset:1232
	s_waitcnt vmcnt(30)
; __device__ __forceinline__ float bf_lo(unsigned w) { return __uint_as_float(w << 16); }
; __device__ __forceinline__ float bf_hi(unsigned w) { return __uint_as_float(w & 0xffff0000u); }
; __global__ void __launch_bounds__(512, 2) fwd_kernel(Params p) {
;     ...
;                 const bf16_t* xr = X1 + (size_t)(blk * 64 + tt * 32 + j) * DM + kq * 512 + hh * 4;
;                 const float* wr_ = WrT + (size_t)j * DM + kq * 512 + hh * 4;
;                 f32x16 acc = {}; float ss = 0.f;
;                 u32x2 xb[2][8]; f32x4 wb[2][8];
; #pragma unroll
;                 for (int i = 0; i < 8; ++i) { xb[0][i] = *(const u32x2*)(xr + i * 8); wb[0][i] = *(const f32x4*)(wr_ + i * 8); }
; #pragma unroll
;                 for (int ch = 0; ch < 8; ++ch) {
;                     if (ch + 1 < 8) {
; #pragma unroll
;                         for (int i = 0; i < 8; ++i) { xb[(ch + 1) & 1][i] = *(const u32x2*)(xr + (ch + 1) * 64 + i * 8); wb[(ch + 1) & 1][i] = *(const f32x4*)(wr_ + (ch + 1) * 64 + i * 8); } }
; #pragma unroll
;                     for (int i = 0; i < 8; ++i) { const u32x2 xp = xb[ch & 1][i]; const f32x4 xv = {bf_lo(xp.x), bf_hi(xp.x), bf_lo(xp.y), bf_hi(xp.y)}, wv = wb[ch & 1][i];
;                         acc = __builtin_amdgcn_mfma_f32_32x32x2f32(wv.x, xv.x, acc, 0, 0, 0); acc = __builtin_amdgcn_mfma_f32_32x32x2f32(wv.y, xv.y, acc, 0, 0, 0);
;                         acc = __builtin_amdgcn_mfma_f32_32x32x2f32(wv.z, xv.z, acc, 0, 0, 0); acc = __builtin_amdgcn_mfma_f32_32x32x2f32(wv.w, xv.w, acc, 0, 0, 0);
;                         ss += (xv.x * xv.x + xv.y * xv.y) + (xv.z * xv.z + xv.w * xv.w); }
;                 }
	v_mfma_f32_32x32x2_f32 v[0:15], v20, v64, v[0:15]
	v_lshlrev_b32_e32 v72, 16, v28
	v_fmac_f32_e32 v80, v64, v64
	v_mfma_f32_32x32x2_f32 v[0:15], v21, v65, v[0:15]
	v_and_b32_e32 v73, 0xffff0000, v28
	v_fmac_f32_e32 v80, v65, v65
	v_mfma_f32_32x32x2_f32 v[0:15], v22, v66, v[0:15]
	v_lshlrev_b32_e32 v74, 16, v29
	v_fmac_f32_e32 v80, v66, v66
	v_mfma_f32_32x32x2_f32 v[0:15], v23, v67, v[0:15]
	v_and_b32_e32 v75, 0xffff0000, v29
	v_fmac_f32_e32 v80, v67, v67
	v_mfma_f32_32x32x2_f32 v[0:15], v24, v68, v[0:15]
	v_lshlrev_b32_e32 v76, 16, v30
	v_fmac_f32_e32 v80, v68, v68
	v_mfma_f32_32x32x2_f32 v[0:15], v25, v69, v[0:15]
	v_and_b32_e32 v77, 0xffff0000, v30
	v_fmac_f32_e32 v80, v69, v69
	v_mfma_f32_32x32x2_f32 v[0:15], v26, v70, v[0:15]
	v_lshlrev_b32_e32 v78, 16, v31
	v_fmac_f32_e32 v80, v70, v70
	v_mfma_f32_32x32x2_f32 v[0:15], v27, v71, v[0:15]
	v_and_b32_e32 v79, 0xffff0000, v31
	v_fmac_f32_e32 v80, v71, v71
	s_waitcnt vmcnt(27)
	v_mfma_f32_32x32x2_f32 v[0:15], v32, v72, v[0:15]
	v_lshlrev_b32_e32 v64, 16, v40
	v_fmac_f32_e32 v80, v72, v72
	v_mfma_f32_32x32x2_f32 v[0:15], v33, v73, v[0:15]
	v_and_b32_e32 v65, 0xffff0000, v40
	v_fmac_f32_e32 v80, v73, v73
	v_mfma_f32_32x32x2_f32 v[0:15], v34, v74, v[0:15]
	v_lshlrev_b32_e32 v66, 16, v41
	v_fmac_f32_e32 v80, v74, v74
	v_mfma_f32_32x32x2_f32 v[0:15], v35, v75, v[0:15]
	v_and_b32_e32 v67, 0xffff0000, v41
	v_fmac_f32_e32 v80, v75, v75
	v_mfma_f32_32x32x2_f32 v[0:15], v36, v76, v[0:15]
	v_lshlrev_b32_e32 v68, 16, v42
	v_fmac_f32_e32 v80, v76, v76
	v_mfma_f32_32x32x2_f32 v[0:15], v37, v77, v[0:15]
	v_and_b32_e32 v69, 0xffff0000, v42
	v_fmac_f32_e32 v80, v77, v77
	v_mfma_f32_32x32x2_f32 v[0:15], v38, v78, v[0:15]
	v_lshlrev_b32_e32 v70, 16, v43
	v_fmac_f32_e32 v80, v78, v78
	v_mfma_f32_32x32x2_f32 v[0:15], v39, v79, v[0:15]
	v_and_b32_e32 v71, 0xffff0000, v43
	v_fmac_f32_e32 v80, v79, v79
	s_waitcnt vmcnt(24)
	v_mfma_f32_32x32x2_f32 v[0:15], v44, v64, v[0:15]
	v_lshlrev_b32_e32 v72, 16, v52
	v_fmac_f32_e32 v80, v64, v64
	v_mfma_f32_32x32x2_f32 v[0:15], v45, v65, v[0:15]
	v_and_b32_e32 v73, 0xffff0000, v52
	v_fmac_f32_e32 v80, v65, v65
	v_mfma_f32_32x32x2_f32 v[0:15], v46, v66, v[0:15]
	v_lshlrev_b32_e32 v74, 16, v53
	v_fmac_f32_e32 v80, v66, v66
	v_mfma_f32_32x32x2_f32 v[0:15], v47, v67, v[0:15]
	v_and_b32_e32 v75, 0xffff0000, v53
	v_fmac_f32_e32 v80, v67, v67
	v_mfma_f32_32x32x2_f32 v[0:15], v48, v68, v[0:15]
	v_lshlrev_b32_e32 v76, 16, v54
	v_fmac_f32_e32 v80, v68, v68
	v_mfma_f32_32x32x2_f32 v[0:15], v49, v69, v[0:15]
	v_and_b32_e32 v77, 0xffff0000, v54
	v_fmac_f32_e32 v80, v69, v69
	v_mfma_f32_32x32x2_f32 v[0:15], v50, v70, v[0:15]
	v_lshlrev_b32_e32 v78, 16, v55
	v_fmac_f32_e32 v80, v70, v70
	v_mfma_f32_32x32x2_f32 v[0:15], v51, v71, v[0:15]
	v_and_b32_e32 v79, 0xffff0000, v55
	v_fmac_f32_e32 v80, v71, v71
	s_waitcnt vmcnt(21)
	v_mfma_f32_32x32x2_f32 v[0:15], v56, v72, v[0:15]
	v_lshlrev_b32_e32 v64, 16, v148
	v_fmac_f32_e32 v80, v72, v72
	v_mfma_f32_32x32x2_f32 v[0:15], v57, v73, v[0:15]
	v_and_b32_e32 v65, 0xffff0000, v148
	v_fmac_f32_e32 v80, v73, v73
	v_mfma_f32_32x32x2_f32 v[0:15], v58, v74, v[0:15]
	v_lshlrev_b32_e32 v66, 16, v149
	v_fmac_f32_e32 v80, v74, v74
	v_mfma_f32_32x32x2_f32 v[0:15], v59, v75, v[0:15]
	v_and_b32_e32 v67, 0xffff0000, v149
	v_fmac_f32_e32 v80, v75, v75
	v_mfma_f32_32x32x2_f32 v[0:15], v60, v76, v[0:15]
	v_lshlrev_b32_e32 v68, 16, v150
	v_fmac_f32_e32 v80, v76, v76
	v_mfma_f32_32x32x2_f32 v[0:15], v61, v77, v[0:15]
	v_and_b32_e32 v69, 0xffff0000, v150
	v_fmac_f32_e32 v80, v77, v77
	v_mfma_f32_32x32x2_f32 v[0:15], v62, v78, v[0:15]
	v_lshlrev_b32_e32 v70, 16, v151
	v_fmac_f32_e32 v80, v78, v78
	v_mfma_f32_32x32x2_f32 v[0:15], v63, v79, v[0:15]
	v_and_b32_e32 v71, 0xffff0000, v151
	v_fmac_f32_e32 v80, v79, v79
	global_load_dwordx4 v[16:19], v[100:101], off offset:640
	global_load_dwordx4 v[20:23], v[102:103], off offset:1280
	global_load_dwordx4 v[24:27], v[102:103], off offset:1296
	global_load_dwordx4 v[28:31], v[100:101], off offset:672
	global_load_dwordx4 v[32:35], v[102:103], off offset:1344
	global_load_dwordx4 v[36:39], v[102:103], off offset:1360
	global_load_dwordx4 v[40:43], v[100:101], off offset:704
	global_load_dwordx4 v[44:47], v[102:103], off offset:1408
	global_load_dwordx4 v[48:51], v[102:103], off offset:1424
	global_load_dwordx4 v[52:55], v[100:101], off offset:736
	global_load_dwordx4 v[56:59], v[102:103], off offset:1472
	global_load_dwordx4 v[60:63], v[102:103], off offset:1488
	s_waitcnt vmcnt(30)
	v_mfma_f32_32x32x2_f32 v[0:15], v152, v64, v[0:15]
	v_lshlrev_b32_e32 v72, 16, v160
	v_fmac_f32_e32 v80, v64, v64
	v_mfma_f32_32x32x2_f32 v[0:15], v153, v65, v[0:15]
	v_and_b32_e32 v73, 0xffff0000, v160
	v_fmac_f32_e32 v80, v65, v65
	v_mfma_f32_32x32x2_f32 v[0:15], v154, v66, v[0:15]
	v_lshlrev_b32_e32 v74, 16, v161
	v_fmac_f32_e32 v80, v66, v66
	v_mfma_f32_32x32x2_f32 v[0:15], v155, v67, v[0:15]
	v_and_b32_e32 v75, 0xffff0000, v161
	v_fmac_f32_e32 v80, v67, v67
	v_mfma_f32_32x32x2_f32 v[0:15], v156, v68, v[0:15]
	v_lshlrev_b32_e32 v76, 16, v162
	v_fmac_f32_e32 v80, v68, v68
	v_mfma_f32_32x32x2_f32 v[0:15], v157, v69, v[0:15]
	v_and_b32_e32 v77, 0xffff0000, v162
	v_fmac_f32_e32 v80, v69, v69
	v_mfma_f32_32x32x2_f32 v[0:15], v158, v70, v[0:15]
	v_lshlrev_b32_e32 v78, 16, v163
	v_fmac_f32_e32 v80, v70, v70
	v_mfma_f32_32x32x2_f32 v[0:15], v159, v71, v[0:15]
	v_and_b32_e32 v79, 0xffff0000, v163
	v_fmac_f32_e32 v80, v71, v71
	s_waitcnt vmcnt(27)
; __device__ __forceinline__ float bf_lo(unsigned w) { return __uint_as_float(w << 16); }
; __device__ __forceinline__ float bf_hi(unsigned w) { return __uint_as_float(w & 0xffff0000u); }
; __global__ void __launch_bounds__(512, 2) fwd_kernel(Params p) {
;     ...
;                 const bf16_t* xr = X1 + (size_t)(blk * 64 + tt * 32 + j) * DM + kq * 512 + hh * 4;
;                 const float* wr_ = WrT + (size_t)j * DM + kq * 512 + hh * 4;
;                 f32x16 acc = {}; float ss = 0.f;
;                 u32x2 xb[2][8]; f32x4 wb[2][8];
; #pragma unroll
;                 for (int i = 0; i < 8; ++i) { xb[0][i] = *(const u32x2*)(xr + i * 8); wb[0][i] = *(const f32x4*)(wr_ + i * 8); }
; #pragma unroll
;                 for (int ch = 0; ch < 8; ++ch) {
;                     if (ch + 1 < 8) {
; #pragma unroll
;                         for (int i = 0; i < 8; ++i) { xb[(ch + 1) & 1][i] = *(const u32x2*)(xr + (ch + 1) * 64 + i * 8); wb[(ch + 1) & 1][i] = *(const f32x4*)(wr_ + (ch + 1) * 64 + i * 8); } }
; #pragma unroll
;                     for (int i = 0; i < 8; ++i) { const u32x2 xp = xb[ch & 1][i]; const f32x4 xv = {bf_lo(xp.x), bf_hi(xp.x), bf_lo(xp.y), bf_hi(xp.y)}, wv = wb[ch & 1][i];
;                         acc = __builtin_amdgcn_mfma_f32_32x32x2f32(wv.x, xv.x, acc, 0, 0, 0); acc = __builtin_amdgcn_mfma_f32_32x32x2f32(wv.y, xv.y, acc, 0, 0, 0);
;                         acc = __builtin_amdgcn_mfma_f32_32x32x2f32(wv.z, xv.z, acc, 0, 0, 0); acc = __builtin_amdgcn_mfma_f32_32x32x2f32(wv.w, xv.w, acc, 0, 0, 0);
;                         ss += (xv.x * xv.x + xv.y * xv.y) + (xv.z * xv.z + xv.w * xv.w); }
;                 }
	v_mfma_f32_32x32x2_f32 v[0:15], v164, v72, v[0:15]
	v_lshlrev_b32_e32 v64, 16, v172
	v_fmac_f32_e32 v80, v72, v72
	v_mfma_f32_32x32x2_f32 v[0:15], v165, v73, v[0:15]
	v_and_b32_e32 v65, 0xffff0000, v172
	v_fmac_f32_e32 v80, v73, v73
	v_mfma_f32_32x32x2_f32 v[0:15], v166, v74, v[0:15]
	v_lshlrev_b32_e32 v66, 16, v173
	v_fmac_f32_e32 v80, v74, v74
	v_mfma_f32_32x32x2_f32 v[0:15], v167, v75, v[0:15]
	v_and_b32_e32 v67, 0xffff0000, v173
	v_fmac_f32_e32 v80, v75, v75
	v_mfma_f32_32x32x2_f32 v[0:15], v168, v76, v[0:15]
	v_lshlrev_b32_e32 v68, 16, v174
	v_fmac_f32_e32 v80, v76, v76
	v_mfma_f32_32x32x2_f32 v[0:15], v169, v77, v[0:15]
	v_and_b32_e32 v69, 0xffff0000, v174
	v_fmac_f32_e32 v80, v77, v77
	v_mfma_f32_32x32x2_f32 v[0:15], v170, v78, v[0:15]
	v_lshlrev_b32_e32 v70, 16, v175
	v_fmac_f32_e32 v80, v78, v78
	v_mfma_f32_32x32x2_f32 v[0:15], v171, v79, v[0:15]
	v_and_b32_e32 v71, 0xffff0000, v175
	v_fmac_f32_e32 v80, v79, v79
	s_waitcnt vmcnt(24)
	v_mfma_f32_32x32x2_f32 v[0:15], v176, v64, v[0:15]
	v_lshlrev_b32_e32 v72, 16, v184
	v_fmac_f32_e32 v80, v64, v64
	v_mfma_f32_32x32x2_f32 v[0:15], v177, v65, v[0:15]
	v_and_b32_e32 v73, 0xffff0000, v184
	v_fmac_f32_e32 v80, v65, v65
	v_mfma_f32_32x32x2_f32 v[0:15], v178, v66, v[0:15]
	v_lshlrev_b32_e32 v74, 16, v185
	v_fmac_f32_e32 v80, v66, v66
	v_mfma_f32_32x32x2_f32 v[0:15], v179, v67, v[0:15]
	v_and_b32_e32 v75, 0xffff0000, v185
	v_fmac_f32_e32 v80, v67, v67
	v_mfma_f32_32x32x2_f32 v[0:15], v180, v68, v[0:15]
	v_lshlrev_b32_e32 v76, 16, v186
	v_fmac_f32_e32 v80, v68, v68
	v_mfma_f32_32x32x2_f32 v[0:15], v181, v69, v[0:15]
	v_and_b32_e32 v77, 0xffff0000, v186
	v_fmac_f32_e32 v80, v69, v69
	v_mfma_f32_32x32x2_f32 v[0:15], v182, v70, v[0:15]
	v_lshlrev_b32_e32 v78, 16, v187
	v_fmac_f32_e32 v80, v70, v70
	v_mfma_f32_32x32x2_f32 v[0:15], v183, v71, v[0:15]
	v_and_b32_e32 v79, 0xffff0000, v187
	v_fmac_f32_e32 v80, v71, v71
	s_waitcnt vmcnt(21)
	v_mfma_f32_32x32x2_f32 v[0:15], v188, v72, v[0:15]
	v_lshlrev_b32_e32 v64, 16, v196
	v_fmac_f32_e32 v80, v72, v72
	v_mfma_f32_32x32x2_f32 v[0:15], v189, v73, v[0:15]
	v_and_b32_e32 v65, 0xffff0000, v196
	v_fmac_f32_e32 v80, v73, v73
	v_mfma_f32_32x32x2_f32 v[0:15], v190, v74, v[0:15]
	v_lshlrev_b32_e32 v66, 16, v197
	v_fmac_f32_e32 v80, v74, v74
	v_mfma_f32_32x32x2_f32 v[0:15], v191, v75, v[0:15]
	v_and_b32_e32 v67, 0xffff0000, v197
	v_fmac_f32_e32 v80, v75, v75
	v_mfma_f32_32x32x2_f32 v[0:15], v192, v76, v[0:15]
	v_lshlrev_b32_e32 v68, 16, v198
	v_fmac_f32_e32 v80, v76, v76
	v_mfma_f32_32x32x2_f32 v[0:15], v193, v77, v[0:15]
	v_and_b32_e32 v69, 0xffff0000, v198
	v_fmac_f32_e32 v80, v77, v77
	v_mfma_f32_32x32x2_f32 v[0:15], v194, v78, v[0:15]
	v_lshlrev_b32_e32 v70, 16, v199
	v_fmac_f32_e32 v80, v78, v78
	v_mfma_f32_32x32x2_f32 v[0:15], v195, v79, v[0:15]
	v_and_b32_e32 v71, 0xffff0000, v199
	v_fmac_f32_e32 v80, v79, v79
	global_load_dwordx4 v[148:151], v[100:101], off offset:768
	global_load_dwordx4 v[152:155], v[102:103], off offset:1536
	global_load_dwordx4 v[156:159], v[102:103], off offset:1552
	global_load_dwordx4 v[160:163], v[100:101], off offset:800
	global_load_dwordx4 v[164:167], v[102:103], off offset:1600
	global_load_dwordx4 v[168:171], v[102:103], off offset:1616
	global_load_dwordx4 v[172:175], v[100:101], off offset:832
	global_load_dwordx4 v[176:179], v[102:103], off offset:1664
	global_load_dwordx4 v[180:183], v[102:103], off offset:1680
	global_load_dwordx4 v[184:187], v[100:101], off offset:864
	global_load_dwordx4 v[188:191], v[102:103], off offset:1728
	global_load_dwordx4 v[192:195], v[102:103], off offset:1744
	s_waitcnt vmcnt(30)
	v_mfma_f32_32x32x2_f32 v[0:15], v200, v64, v[0:15]
	v_lshlrev_b32_e32 v72, 16, v208
	v_fmac_f32_e32 v80, v64, v64
	v_mfma_f32_32x32x2_f32 v[0:15], v201, v65, v[0:15]
	v_and_b32_e32 v73, 0xffff0000, v208
	v_fmac_f32_e32 v80, v65, v65
	v_mfma_f32_32x32x2_f32 v[0:15], v202, v66, v[0:15]
	v_lshlrev_b32_e32 v74, 16, v209
	v_fmac_f32_e32 v80, v66, v66
	v_mfma_f32_32x32x2_f32 v[0:15], v203, v67, v[0:15]
	v_and_b32_e32 v75, 0xffff0000, v209
	v_fmac_f32_e32 v80, v67, v67
	v_mfma_f32_32x32x2_f32 v[0:15], v204, v68, v[0:15]
	v_lshlrev_b32_e32 v76, 16, v210
	v_fmac_f32_e32 v80, v68, v68
	v_mfma_f32_32x32x2_f32 v[0:15], v205, v69, v[0:15]
	v_and_b32_e32 v77, 0xffff0000, v210
	v_fmac_f32_e32 v80, v69, v69
	v_mfma_f32_32x32x2_f32 v[0:15], v206, v70, v[0:15]
	v_lshlrev_b32_e32 v78, 16, v211
	v_fmac_f32_e32 v80, v70, v70
	v_mfma_f32_32x32x2_f32 v[0:15], v207, v71, v[0:15]
	v_and_b32_e32 v79, 0xffff0000, v211
	v_fmac_f32_e32 v80, v71, v71
	s_waitcnt vmcnt(27)
	v_mfma_f32_32x32x2_f32 v[0:15], v212, v72, v[0:15]
	v_lshlrev_b32_e32 v64, 16, v220
	v_fmac_f32_e32 v80, v72, v72
	v_mfma_f32_32x32x2_f32 v[0:15], v213, v73, v[0:15]
	v_and_b32_e32 v65, 0xffff0000, v220
	v_fmac_f32_e32 v80, v73, v73
	v_mfma_f32_32x32x2_f32 v[0:15], v214, v74, v[0:15]
	v_lshlrev_b32_e32 v66, 16, v221
	v_fmac_f32_e32 v80, v74, v74
	v_mfma_f32_32x32x2_f32 v[0:15], v215, v75, v[0:15]
	v_and_b32_e32 v67, 0xffff0000, v221
	v_fmac_f32_e32 v80, v75, v75
	v_mfma_f32_32x32x2_f32 v[0:15], v216, v76, v[0:15]
	v_lshlrev_b32_e32 v68, 16, v222
	v_fmac_f32_e32 v80, v76, v76
	v_mfma_f32_32x32x2_f32 v[0:15], v217, v77, v[0:15]
	v_and_b32_e32 v69, 0xffff0000, v222
	v_fmac_f32_e32 v80, v77, v77
	v_mfma_f32_32x32x2_f32 v[0:15], v218, v78, v[0:15]
	v_lshlrev_b32_e32 v70, 16, v223
	v_fmac_f32_e32 v80, v78, v78
	v_mfma_f32_32x32x2_f32 v[0:15], v219, v79, v[0:15]
	v_and_b32_e32 v71, 0xffff0000, v223
	v_fmac_f32_e32 v80, v79, v79
	s_waitcnt vmcnt(24)
; __device__ __forceinline__ float bf_lo(unsigned w) { return __uint_as_float(w << 16); }
; __device__ __forceinline__ float bf_hi(unsigned w) { return __uint_as_float(w & 0xffff0000u); }
; __global__ void __launch_bounds__(512, 2) fwd_kernel(Params p) {
;     ...
;                 const bf16_t* xr = X1 + (size_t)(blk * 64 + tt * 32 + j) * DM + kq * 512 + hh * 4;
;                 const float* wr_ = WrT + (size_t)j * DM + kq * 512 + hh * 4;
;                 f32x16 acc = {}; float ss = 0.f;
;                 u32x2 xb[2][8]; f32x4 wb[2][8];
; #pragma unroll
;                 for (int i = 0; i < 8; ++i) { xb[0][i] = *(const u32x2*)(xr + i * 8); wb[0][i] = *(const f32x4*)(wr_ + i * 8); }
; #pragma unroll
;                 for (int ch = 0; ch < 8; ++ch) {
;                     if (ch + 1 < 8) {
; #pragma unroll
;                         for (int i = 0; i < 8; ++i) { xb[(ch + 1) & 1][i] = *(const u32x2*)(xr + (ch + 1) * 64 + i * 8); wb[(ch + 1) & 1][i] = *(const f32x4*)(wr_ + (ch + 1) * 64 + i * 8); } }
; #pragma unroll
;                     for (int i = 0; i < 8; ++i) { const u32x2 xp = xb[ch & 1][i]; const f32x4 xv = {bf_lo(xp.x), bf_hi(xp.x), bf_lo(xp.y), bf_hi(xp.y)}, wv = wb[ch & 1][i];
;                         acc = __builtin_amdgcn_mfma_f32_32x32x2f32(wv.x, xv.x, acc, 0, 0, 0); acc = __builtin_amdgcn_mfma_f32_32x32x2f32(wv.y, xv.y, acc, 0, 0, 0);
;                         acc = __builtin_amdgcn_mfma_f32_32x32x2f32(wv.z, xv.z, acc, 0, 0, 0); acc = __builtin_amdgcn_mfma_f32_32x32x2f32(wv.w, xv.w, acc, 0, 0, 0);
;                         ss += (xv.x * xv.x + xv.y * xv.y) + (xv.z * xv.z + xv.w * xv.w); }
;                 }
	v_mfma_f32_32x32x2_f32 v[0:15], v224, v64, v[0:15]
	v_lshlrev_b32_e32 v72, 16, v232
	v_fmac_f32_e32 v80, v64, v64
	v_mfma_f32_32x32x2_f32 v[0:15], v225, v65, v[0:15]
	v_and_b32_e32 v73, 0xffff0000, v232
	v_fmac_f32_e32 v80, v65, v65
	v_mfma_f32_32x32x2_f32 v[0:15], v226, v66, v[0:15]
	v_lshlrev_b32_e32 v74, 16, v233
	v_fmac_f32_e32 v80, v66, v66
	v_mfma_f32_32x32x2_f32 v[0:15], v227, v67, v[0:15]
	v_and_b32_e32 v75, 0xffff0000, v233
	v_fmac_f32_e32 v80, v67, v67
	v_mfma_f32_32x32x2_f32 v[0:15], v228, v68, v[0:15]
	v_lshlrev_b32_e32 v76, 16, v234
	v_fmac_f32_e32 v80, v68, v68
	v_mfma_f32_32x32x2_f32 v[0:15], v229, v69, v[0:15]
	v_and_b32_e32 v77, 0xffff0000, v234
	v_fmac_f32_e32 v80, v69, v69
	v_mfma_f32_32x32x2_f32 v[0:15], v230, v70, v[0:15]
	v_lshlrev_b32_e32 v78, 16, v235
	v_fmac_f32_e32 v80, v70, v70
	v_mfma_f32_32x32x2_f32 v[0:15], v231, v71, v[0:15]
	v_and_b32_e32 v79, 0xffff0000, v235
	v_fmac_f32_e32 v80, v71, v71
	s_waitcnt vmcnt(21)
	v_mfma_f32_32x32x2_f32 v[0:15], v236, v72, v[0:15]
	v_lshlrev_b32_e32 v64, 16, v16
	v_fmac_f32_e32 v80, v72, v72
	v_mfma_f32_32x32x2_f32 v[0:15], v237, v73, v[0:15]
	v_and_b32_e32 v65, 0xffff0000, v16
	v_fmac_f32_e32 v80, v73, v73
	v_mfma_f32_32x32x2_f32 v[0:15], v238, v74, v[0:15]
	v_lshlrev_b32_e32 v66, 16, v17
	v_fmac_f32_e32 v80, v74, v74
	v_mfma_f32_32x32x2_f32 v[0:15], v239, v75, v[0:15]
	v_and_b32_e32 v67, 0xffff0000, v17
	v_fmac_f32_e32 v80, v75, v75
	v_mfma_f32_32x32x2_f32 v[0:15], v240, v76, v[0:15]
	v_lshlrev_b32_e32 v68, 16, v18
	v_fmac_f32_e32 v80, v76, v76
	v_mfma_f32_32x32x2_f32 v[0:15], v241, v77, v[0:15]
	v_and_b32_e32 v69, 0xffff0000, v18
	v_fmac_f32_e32 v80, v77, v77
	v_mfma_f32_32x32x2_f32 v[0:15], v242, v78, v[0:15]
	v_lshlrev_b32_e32 v70, 16, v19
	v_fmac_f32_e32 v80, v78, v78
	v_mfma_f32_32x32x2_f32 v[0:15], v243, v79, v[0:15]
	v_and_b32_e32 v71, 0xffff0000, v19
	v_fmac_f32_e32 v80, v79, v79
	global_load_dwordx4 v[196:199], v[100:101], off offset:896
	global_load_dwordx4 v[200:203], v[102:103], off offset:1792
	global_load_dwordx4 v[204:207], v[102:103], off offset:1808
	global_load_dwordx4 v[208:211], v[100:101], off offset:928
	global_load_dwordx4 v[212:215], v[102:103], off offset:1856
	global_load_dwordx4 v[216:219], v[102:103], off offset:1872
	global_load_dwordx4 v[220:223], v[100:101], off offset:960
	global_load_dwordx4 v[224:227], v[102:103], off offset:1920
	global_load_dwordx4 v[228:231], v[102:103], off offset:1936
	global_load_dwordx4 v[232:235], v[100:101], off offset:992
	global_load_dwordx4 v[236:239], v[102:103], off offset:1984
	global_load_dwordx4 v[240:243], v[102:103], off offset:2000
	s_waitcnt vmcnt(30)
	v_mfma_f32_32x32x2_f32 v[0:15], v20, v64, v[0:15]
	v_lshlrev_b32_e32 v72, 16, v28
	v_fmac_f32_e32 v80, v64, v64
	v_mfma_f32_32x32x2_f32 v[0:15], v21, v65, v[0:15]
	v_and_b32_e32 v73, 0xffff0000, v28
	v_fmac_f32_e32 v80, v65, v65
	v_mfma_f32_32x32x2_f32 v[0:15], v22, v66, v[0:15]
	v_lshlrev_b32_e32 v74, 16, v29
	v_fmac_f32_e32 v80, v66, v66
	v_mfma_f32_32x32x2_f32 v[0:15], v23, v67, v[0:15]
	v_and_b32_e32 v75, 0xffff0000, v29
	v_fmac_f32_e32 v80, v67, v67
	v_mfma_f32_32x32x2_f32 v[0:15], v24, v68, v[0:15]
	v_lshlrev_b32_e32 v76, 16, v30
	v_fmac_f32_e32 v80, v68, v68
	v_mfma_f32_32x32x2_f32 v[0:15], v25, v69, v[0:15]
	v_and_b32_e32 v77, 0xffff0000, v30
	v_fmac_f32_e32 v80, v69, v69
	v_mfma_f32_32x32x2_f32 v[0:15], v26, v70, v[0:15]
	v_lshlrev_b32_e32 v78, 16, v31
	v_fmac_f32_e32 v80, v70, v70
	v_mfma_f32_32x32x2_f32 v[0:15], v27, v71, v[0:15]
	v_and_b32_e32 v79, 0xffff0000, v31
	v_fmac_f32_e32 v80, v71, v71
	s_waitcnt vmcnt(27)
	v_mfma_f32_32x32x2_f32 v[0:15], v32, v72, v[0:15]
	v_lshlrev_b32_e32 v64, 16, v40
	v_fmac_f32_e32 v80, v72, v72
	v_mfma_f32_32x32x2_f32 v[0:15], v33, v73, v[0:15]
	v_and_b32_e32 v65, 0xffff0000, v40
	v_fmac_f32_e32 v80, v73, v73
	v_mfma_f32_32x32x2_f32 v[0:15], v34, v74, v[0:15]
	v_lshlrev_b32_e32 v66, 16, v41
	v_fmac_f32_e32 v80, v74, v74
	v_mfma_f32_32x32x2_f32 v[0:15], v35, v75, v[0:15]
	v_and_b32_e32 v67, 0xffff0000, v41
	v_fmac_f32_e32 v80, v75, v75
	v_mfma_f32_32x32x2_f32 v[0:15], v36, v76, v[0:15]
	v_lshlrev_b32_e32 v68, 16, v42
	v_fmac_f32_e32 v80, v76, v76
	v_mfma_f32_32x32x2_f32 v[0:15], v37, v77, v[0:15]
	v_and_b32_e32 v69, 0xffff0000, v42
	v_fmac_f32_e32 v80, v77, v77
	v_mfma_f32_32x32x2_f32 v[0:15], v38, v78, v[0:15]
	v_lshlrev_b32_e32 v70, 16, v43
	v_fmac_f32_e32 v80, v78, v78
	v_mfma_f32_32x32x2_f32 v[0:15], v39, v79, v[0:15]
	v_and_b32_e32 v71, 0xffff0000, v43
	v_fmac_f32_e32 v80, v79, v79
	s_waitcnt vmcnt(24)
	v_mfma_f32_32x32x2_f32 v[0:15], v44, v64, v[0:15]
	v_lshlrev_b32_e32 v72, 16, v52
	v_fmac_f32_e32 v80, v64, v64
	v_mfma_f32_32x32x2_f32 v[0:15], v45, v65, v[0:15]
	v_and_b32_e32 v73, 0xffff0000, v52
	v_fmac_f32_e32 v80, v65, v65
	v_mfma_f32_32x32x2_f32 v[0:15], v46, v66, v[0:15]
	v_lshlrev_b32_e32 v74, 16, v53
	v_fmac_f32_e32 v80, v66, v66
	v_mfma_f32_32x32x2_f32 v[0:15], v47, v67, v[0:15]
	v_and_b32_e32 v75, 0xffff0000, v53
	v_fmac_f32_e32 v80, v67, v67
	v_mfma_f32_32x32x2_f32 v[0:15], v48, v68, v[0:15]
	v_lshlrev_b32_e32 v76, 16, v54
	v_fmac_f32_e32 v80, v68, v68
	v_mfma_f32_32x32x2_f32 v[0:15], v49, v69, v[0:15]
	v_and_b32_e32 v77, 0xffff0000, v54
	v_fmac_f32_e32 v80, v69, v69
	v_mfma_f32_32x32x2_f32 v[0:15], v50, v70, v[0:15]
	v_lshlrev_b32_e32 v78, 16, v55
	v_fmac_f32_e32 v80, v70, v70
	v_mfma_f32_32x32x2_f32 v[0:15], v51, v71, v[0:15]
	v_and_b32_e32 v79, 0xffff0000, v55
	v_fmac_f32_e32 v80, v71, v71
	s_waitcnt vmcnt(21)
; __device__ __forceinline__ float bf_lo(unsigned w) { return __uint_as_float(w << 16); }
; __device__ __forceinline__ float bf_hi(unsigned w) { return __uint_as_float(w & 0xffff0000u); }
; __global__ void __launch_bounds__(512, 2) fwd_kernel(Params p) {
;     ...
;                 const bf16_t* xr = X1 + (size_t)(blk * 64 + tt * 32 + j) * DM + kq * 512 + hh * 4;
;                 const float* wr_ = WrT + (size_t)j * DM + kq * 512 + hh * 4;
;                 f32x16 acc = {}; float ss = 0.f;
;                 u32x2 xb[2][8]; f32x4 wb[2][8];
; #pragma unroll
;                 for (int i = 0; i < 8; ++i) { xb[0][i] = *(const u32x2*)(xr + i * 8); wb[0][i] = *(const f32x4*)(wr_ + i * 8); }
; #pragma unroll
;                 for (int ch = 0; ch < 8; ++ch) {
;                     if (ch + 1 < 8) {
; #pragma unroll
;                         for (int i = 0; i < 8; ++i) { xb[(ch + 1) & 1][i] = *(const u32x2*)(xr + (ch + 1) * 64 + i * 8); wb[(ch + 1) & 1][i] = *(const f32x4*)(wr_ + (ch + 1) * 64 + i * 8); } }
; #pragma unroll
;                     for (int i = 0; i < 8; ++i) { const u32x2 xp = xb[ch & 1][i]; const f32x4 xv = {bf_lo(xp.x), bf_hi(xp.x), bf_lo(xp.y), bf_hi(xp.y)}, wv = wb[ch & 1][i];
;                         acc = __builtin_amdgcn_mfma_f32_32x32x2f32(wv.x, xv.x, acc, 0, 0, 0); acc = __builtin_amdgcn_mfma_f32_32x32x2f32(wv.y, xv.y, acc, 0, 0, 0);
;                         acc = __builtin_amdgcn_mfma_f32_32x32x2f32(wv.z, xv.z, acc, 0, 0, 0); acc = __builtin_amdgcn_mfma_f32_32x32x2f32(wv.w, xv.w, acc, 0, 0, 0);
;                         ss += (xv.x * xv.x + xv.y * xv.y) + (xv.z * xv.z + xv.w * xv.w); }
;                 }
	v_mfma_f32_32x32x2_f32 v[0:15], v56, v72, v[0:15]
	v_lshlrev_b32_e32 v64, 16, v148
	v_fmac_f32_e32 v80, v72, v72
	v_mfma_f32_32x32x2_f32 v[0:15], v57, v73, v[0:15]
	v_and_b32_e32 v65, 0xffff0000, v148
	v_fmac_f32_e32 v80, v73, v73
	v_mfma_f32_32x32x2_f32 v[0:15], v58, v74, v[0:15]
	v_lshlrev_b32_e32 v66, 16, v149
	v_fmac_f32_e32 v80, v74, v74
	v_mfma_f32_32x32x2_f32 v[0:15], v59, v75, v[0:15]
	v_and_b32_e32 v67, 0xffff0000, v149
	v_fmac_f32_e32 v80, v75, v75
	v_mfma_f32_32x32x2_f32 v[0:15], v60, v76, v[0:15]
	v_lshlrev_b32_e32 v68, 16, v150
	v_fmac_f32_e32 v80, v76, v76
	v_mfma_f32_32x32x2_f32 v[0:15], v61, v77, v[0:15]
	v_and_b32_e32 v69, 0xffff0000, v150
	v_fmac_f32_e32 v80, v77, v77
	v_mfma_f32_32x32x2_f32 v[0:15], v62, v78, v[0:15]
	v_lshlrev_b32_e32 v70, 16, v151
	v_fmac_f32_e32 v80, v78, v78
	v_mfma_f32_32x32x2_f32 v[0:15], v63, v79, v[0:15]
	v_and_b32_e32 v71, 0xffff0000, v151
	v_fmac_f32_e32 v80, v79, v79
	s_waitcnt vmcnt(18)
	v_mfma_f32_32x32x2_f32 v[0:15], v152, v64, v[0:15]
	v_lshlrev_b32_e32 v72, 16, v160
	v_fmac_f32_e32 v80, v64, v64
	v_mfma_f32_32x32x2_f32 v[0:15], v153, v65, v[0:15]
	v_and_b32_e32 v73, 0xffff0000, v160
	v_fmac_f32_e32 v80, v65, v65
	v_mfma_f32_32x32x2_f32 v[0:15], v154, v66, v[0:15]
	v_lshlrev_b32_e32 v74, 16, v161
	v_fmac_f32_e32 v80, v66, v66
	v_mfma_f32_32x32x2_f32 v[0:15], v155, v67, v[0:15]
	v_and_b32_e32 v75, 0xffff0000, v161
	v_fmac_f32_e32 v80, v67, v67
	v_mfma_f32_32x32x2_f32 v[0:15], v156, v68, v[0:15]
	v_lshlrev_b32_e32 v76, 16, v162
	v_fmac_f32_e32 v80, v68, v68
	v_mfma_f32_32x32x2_f32 v[0:15], v157, v69, v[0:15]
	v_and_b32_e32 v77, 0xffff0000, v162
	v_fmac_f32_e32 v80, v69, v69
	v_mfma_f32_32x32x2_f32 v[0:15], v158, v70, v[0:15]
	v_lshlrev_b32_e32 v78, 16, v163
	v_fmac_f32_e32 v80, v70, v70
	v_mfma_f32_32x32x2_f32 v[0:15], v159, v71, v[0:15]
	v_and_b32_e32 v79, 0xffff0000, v163
	v_fmac_f32_e32 v80, v71, v71
	s_waitcnt vmcnt(15)
	v_mfma_f32_32x32x2_f32 v[0:15], v164, v72, v[0:15]
	v_lshlrev_b32_e32 v64, 16, v172
	v_fmac_f32_e32 v80, v72, v72
	v_mfma_f32_32x32x2_f32 v[0:15], v165, v73, v[0:15]
	v_and_b32_e32 v65, 0xffff0000, v172
	v_fmac_f32_e32 v80, v73, v73
	v_mfma_f32_32x32x2_f32 v[0:15], v166, v74, v[0:15]
	v_lshlrev_b32_e32 v66, 16, v173
	v_fmac_f32_e32 v80, v74, v74
	v_mfma_f32_32x32x2_f32 v[0:15], v167, v75, v[0:15]
	v_and_b32_e32 v67, 0xffff0000, v173
	v_fmac_f32_e32 v80, v75, v75
	v_mfma_f32_32x32x2_f32 v[0:15], v168, v76, v[0:15]
	v_lshlrev_b32_e32 v68, 16, v174
	v_fmac_f32_e32 v80, v76, v76
	v_mfma_f32_32x32x2_f32 v[0:15], v169, v77, v[0:15]
	v_and_b32_e32 v69, 0xffff0000, v174
	v_fmac_f32_e32 v80, v77, v77
	v_mfma_f32_32x32x2_f32 v[0:15], v170, v78, v[0:15]
	v_lshlrev_b32_e32 v70, 16, v175
	v_fmac_f32_e32 v80, v78, v78
	v_mfma_f32_32x32x2_f32 v[0:15], v171, v79, v[0:15]
	v_and_b32_e32 v71, 0xffff0000, v175
	v_fmac_f32_e32 v80, v79, v79
	s_waitcnt vmcnt(12)
	v_mfma_f32_32x32x2_f32 v[0:15], v176, v64, v[0:15]
	v_lshlrev_b32_e32 v72, 16, v184
	v_fmac_f32_e32 v80, v64, v64
	v_mfma_f32_32x32x2_f32 v[0:15], v177, v65, v[0:15]
	v_and_b32_e32 v73, 0xffff0000, v184
	v_fmac_f32_e32 v80, v65, v65
	v_mfma_f32_32x32x2_f32 v[0:15], v178, v66, v[0:15]
	v_lshlrev_b32_e32 v74, 16, v185
	v_fmac_f32_e32 v80, v66, v66
	v_mfma_f32_32x32x2_f32 v[0:15], v179, v67, v[0:15]
	v_and_b32_e32 v75, 0xffff0000, v185
	v_fmac_f32_e32 v80, v67, v67
	v_mfma_f32_32x32x2_f32 v[0:15], v180, v68, v[0:15]
	v_lshlrev_b32_e32 v76, 16, v186
	v_fmac_f32_e32 v80, v68, v68
	v_mfma_f32_32x32x2_f32 v[0:15], v181, v69, v[0:15]
	v_and_b32_e32 v77, 0xffff0000, v186
	v_fmac_f32_e32 v80, v69, v69
	v_mfma_f32_32x32x2_f32 v[0:15], v182, v70, v[0:15]
	v_lshlrev_b32_e32 v78, 16, v187
	v_fmac_f32_e32 v80, v70, v70
	v_mfma_f32_32x32x2_f32 v[0:15], v183, v71, v[0:15]
	v_and_b32_e32 v79, 0xffff0000, v187
	v_fmac_f32_e32 v80, v71, v71
	s_waitcnt vmcnt(9)
	v_mfma_f32_32x32x2_f32 v[0:15], v188, v72, v[0:15]
	v_lshlrev_b32_e32 v64, 16, v196
	v_fmac_f32_e32 v80, v72, v72
	v_mfma_f32_32x32x2_f32 v[0:15], v189, v73, v[0:15]
	v_and_b32_e32 v65, 0xffff0000, v196
	v_fmac_f32_e32 v80, v73, v73
	v_mfma_f32_32x32x2_f32 v[0:15], v190, v74, v[0:15]
	v_lshlrev_b32_e32 v66, 16, v197
	v_fmac_f32_e32 v80, v74, v74
	v_mfma_f32_32x32x2_f32 v[0:15], v191, v75, v[0:15]
	v_and_b32_e32 v67, 0xffff0000, v197
	v_fmac_f32_e32 v80, v75, v75
	v_mfma_f32_32x32x2_f32 v[0:15], v192, v76, v[0:15]
	v_lshlrev_b32_e32 v68, 16, v198
	v_fmac_f32_e32 v80, v76, v76
	v_mfma_f32_32x32x2_f32 v[0:15], v193, v77, v[0:15]
	v_and_b32_e32 v69, 0xffff0000, v198
	v_fmac_f32_e32 v80, v77, v77
	v_mfma_f32_32x32x2_f32 v[0:15], v194, v78, v[0:15]
	v_lshlrev_b32_e32 v70, 16, v199
	v_fmac_f32_e32 v80, v78, v78
	v_mfma_f32_32x32x2_f32 v[0:15], v195, v79, v[0:15]
	v_and_b32_e32 v71, 0xffff0000, v199
	v_fmac_f32_e32 v80, v79, v79
	s_waitcnt vmcnt(6)
	v_mfma_f32_32x32x2_f32 v[0:15], v200, v64, v[0:15]
	v_lshlrev_b32_e32 v72, 16, v208
	v_fmac_f32_e32 v80, v64, v64
	v_mfma_f32_32x32x2_f32 v[0:15], v201, v65, v[0:15]
	v_and_b32_e32 v73, 0xffff0000, v208
	v_fmac_f32_e32 v80, v65, v65
	v_mfma_f32_32x32x2_f32 v[0:15], v202, v66, v[0:15]
	v_lshlrev_b32_e32 v74, 16, v209
	v_fmac_f32_e32 v80, v66, v66
	v_mfma_f32_32x32x2_f32 v[0:15], v203, v67, v[0:15]
	v_and_b32_e32 v75, 0xffff0000, v209
	v_fmac_f32_e32 v80, v67, v67
	v_mfma_f32_32x32x2_f32 v[0:15], v204, v68, v[0:15]
	v_lshlrev_b32_e32 v76, 16, v210
	v_fmac_f32_e32 v80, v68, v68
	v_mfma_f32_32x32x2_f32 v[0:15], v205, v69, v[0:15]
	v_and_b32_e32 v77, 0xffff0000, v210
	v_fmac_f32_e32 v80, v69, v69
	v_mfma_f32_32x32x2_f32 v[0:15], v206, v70, v[0:15]
	v_lshlrev_b32_e32 v78, 16, v211
	v_fmac_f32_e32 v80, v70, v70
	v_mfma_f32_32x32x2_f32 v[0:15], v207, v71, v[0:15]
	v_and_b32_e32 v79, 0xffff0000, v211
	v_fmac_f32_e32 v80, v71, v71
	s_waitcnt vmcnt(3)
; #define LAS __attribute__((address_space(3)))
; __global__ void __launch_bounds__(512, 2) fwd_kernel(Params p) {
;     ...
;                 }
;                 LAS float* pp = part + ((kq * 2 + tt) * 32 + j) * 33;
; #pragma unroll
;                 for (int r = 0; r < 16; ++r) pp[(r & 3) + 8 * (r >> 2) + 4 * hh] = acc[r];
;                 ssq[((kq * 2 + tt) * 32 + j) * 2 + hh] = ss;
;             }
;             __syncthreads();
;             int te[4];
;             if (tid < 64) {
;                 const int t2 = tid >> 5, jj = tid & 31, tok = blk * 64 + tid;
;                 float s = 0.f;
; #pragma unroll
;                 for (int q = 0; q < 4; ++q) s += ssq[((q * 2 + t2) * 32 + jj) * 2] + ssq[((q * 2 + t2) * 32 + jj) * 2 + 1];
;                 const float rstd = rsqrtf(s * (1.f / DM) + RMS_EPS);
;                 RS2[tok] = rstd;
	v_mfma_f32_32x32x2_f32 v[0:15], v212, v72, v[0:15]
	v_lshlrev_b32_e32 v64, 16, v220
	v_fmac_f32_e32 v80, v72, v72
	v_mfma_f32_32x32x2_f32 v[0:15], v213, v73, v[0:15]
	v_and_b32_e32 v65, 0xffff0000, v220
	v_fmac_f32_e32 v80, v73, v73
	v_mfma_f32_32x32x2_f32 v[0:15], v214, v74, v[0:15]
	v_lshlrev_b32_e32 v66, 16, v221
	v_fmac_f32_e32 v80, v74, v74
	v_mfma_f32_32x32x2_f32 v[0:15], v215, v75, v[0:15]
	v_and_b32_e32 v67, 0xffff0000, v221
	v_fmac_f32_e32 v80, v75, v75
	v_mfma_f32_32x32x2_f32 v[0:15], v216, v76, v[0:15]
	v_lshlrev_b32_e32 v68, 16, v222
	v_fmac_f32_e32 v80, v76, v76
	v_mfma_f32_32x32x2_f32 v[0:15], v217, v77, v[0:15]
	v_and_b32_e32 v69, 0xffff0000, v222
	v_fmac_f32_e32 v80, v77, v77
	v_mfma_f32_32x32x2_f32 v[0:15], v218, v78, v[0:15]
	v_lshlrev_b32_e32 v70, 16, v223
	v_fmac_f32_e32 v80, v78, v78
	v_mfma_f32_32x32x2_f32 v[0:15], v219, v79, v[0:15]
	v_and_b32_e32 v71, 0xffff0000, v223
	v_fmac_f32_e32 v80, v79, v79
	s_waitcnt vmcnt(0)
	v_mfma_f32_32x32x2_f32 v[0:15], v224, v64, v[0:15]
	v_lshlrev_b32_e32 v72, 16, v232
	v_fmac_f32_e32 v80, v64, v64
	v_mfma_f32_32x32x2_f32 v[0:15], v225, v65, v[0:15]
	v_and_b32_e32 v73, 0xffff0000, v232
	v_fmac_f32_e32 v80, v65, v65
	v_mfma_f32_32x32x2_f32 v[0:15], v226, v66, v[0:15]
	v_lshlrev_b32_e32 v74, 16, v233
	v_fmac_f32_e32 v80, v66, v66
	v_mfma_f32_32x32x2_f32 v[0:15], v227, v67, v[0:15]
	v_and_b32_e32 v75, 0xffff0000, v233
	v_fmac_f32_e32 v80, v67, v67
	v_mfma_f32_32x32x2_f32 v[0:15], v228, v68, v[0:15]
	v_lshlrev_b32_e32 v76, 16, v234
	v_fmac_f32_e32 v80, v68, v68
	v_mfma_f32_32x32x2_f32 v[0:15], v229, v69, v[0:15]
	v_and_b32_e32 v77, 0xffff0000, v234
	v_fmac_f32_e32 v80, v69, v69
	v_mfma_f32_32x32x2_f32 v[0:15], v230, v70, v[0:15]
	v_lshlrev_b32_e32 v78, 16, v235
	v_fmac_f32_e32 v80, v70, v70
	v_mfma_f32_32x32x2_f32 v[0:15], v231, v71, v[0:15]
	v_and_b32_e32 v79, 0xffff0000, v235
	v_fmac_f32_e32 v80, v71, v71
	v_mfma_f32_32x32x2_f32 v[0:15], v236, v72, v[0:15]
	v_fmac_f32_e32 v80, v72, v72
	v_mfma_f32_32x32x2_f32 v[0:15], v237, v73, v[0:15]
	v_fmac_f32_e32 v80, v73, v73
	v_mfma_f32_32x32x2_f32 v[0:15], v238, v74, v[0:15]
	v_fmac_f32_e32 v80, v74, v74
	v_mfma_f32_32x32x2_f32 v[0:15], v239, v75, v[0:15]
	v_fmac_f32_e32 v80, v75, v75
	v_mfma_f32_32x32x2_f32 v[0:15], v240, v76, v[0:15]
	v_fmac_f32_e32 v80, v76, v76
	v_mfma_f32_32x32x2_f32 v[0:15], v241, v77, v[0:15]
	v_fmac_f32_e32 v80, v77, v77
	v_mfma_f32_32x32x2_f32 v[0:15], v242, v78, v[0:15]
	v_fmac_f32_e32 v80, v78, v78
	v_mfma_f32_32x32x2_f32 v[0:15], v243, v79, v[0:15]
	v_fmac_f32_e32 v80, v79, v79
	s_nop 15
	s_nop 1
	ds_write2_b32 v85, v0, v1 offset1:1
	ds_write2_b32 v85, v2, v3 offset0:2 offset1:3
	ds_write2_b32 v85, v4, v5 offset0:8 offset1:9
	ds_write2_b32 v85, v6, v7 offset0:10 offset1:11
	ds_write2_b32 v85, v8, v9 offset0:16 offset1:17
	ds_write2_b32 v85, v10, v11 offset0:18 offset1:19
	ds_write2_b32 v85, v12, v13 offset0:24 offset1:25
	ds_write2_b32 v85, v14, v15 offset0:26 offset1:27
	v_mov_b32_e32 v0, v80
	v_add_u32_e32 v34, s10, v84
	v_ashrrev_i32_e32 v35, 31, v34
	ds_write_b32 v86, v0 offset:36864
	global_load_dwordx4 v[200:203], v87, s[38:39] offset:48
	global_load_dwordx4 v[204:207], v87, s[38:39] offset:32
	global_load_dwordx4 v[208:211], v87, s[38:39] offset:16
	global_load_dwordx4 v[212:215], v87, s[38:39]
	global_load_dwordx4 v[216:219], v87, s[38:39] offset:112
	global_load_dwordx4 v[220:223], v87, s[38:39] offset:96
	global_load_dwordx4 v[224:227], v87, s[38:39] offset:80
	global_load_dwordx4 v[228:231], v87, s[38:39] offset:64
	s_waitcnt lgkmcnt(0)
	s_barrier
	s_and_saveexec_b64 s[46:47], s[6:7]
	s_cbranch_execz .LBB0_986
	ds_read2st64_b64 v[0:3], v136 offset0:72 offset1:73
	ds_read2_b32 v[18:19], v135 offset1:1
	s_movk_i32 s0, 0x80
	s_waitcnt lgkmcnt(1)
	v_mov_b32_e32 v4, v0
	v_mov_b32_e32 v5, v2
	v_mov_b32_e32 v2, v1
	v_pk_add_f32 v[0:1], v[4:5], v[2:3]
	s_nop 0
	v_add_f32_e32 v0, 0, v0
	v_add_f32_e32 v6, v0, v1
	ds_read2st64_b64 v[0:3], v136 offset0:74 offset1:75
	s_waitcnt lgkmcnt(0)
	v_mov_b32_e32 v4, v0
	v_mov_b32_e32 v5, v2
	v_mov_b32_e32 v2, v1
	v_pk_add_f32 v[0:1], v[4:5], v[2:3]
	s_nop 0
	v_add_f32_e32 v0, v6, v0
	v_add_f32_e32 v0, v0, v1
	v_fmamk_f32 v0, v0, 0x3a000000, v137
	v_cmp_gt_f32_e32 vcc, s57, v0
	v_mul_f32_e32 v1, 0x4b800000, v0
	s_nop 0
	v_cndmask_b32_e32 v0, v0, v1, vcc
	v_rsq_f32_e32 v0, v0
	s_nop 0
	v_mul_f32_e32 v1, 0x45800000, v0
	v_cndmask_b32_e32 v16, v0, v1, vcc
	v_mov_b32_e32 v244, v16
	v_lshl_add_u64 v[0:1], v[34:35], 2, s[44:45]
	global_store_dword v[0:1], v16, off
	v_add_u32_e32 v1, 0x2100, v135
	ds_read2_b32 v[20:21], v1 offset1:1
	v_add_u32_e32 v1, 0x4200, v135
	ds_read2_b32 v[22:23], v1 offset1:1
	v_add_u32_e32 v1, 0x6300, v135
	ds_read2_b32 v[24:25], v1 offset1:1
	v_add_f32_e32 v0, 0, v18
	s_waitcnt lgkmcnt(2)
	v_add_f32_e32 v0, v0, v20
	s_waitcnt lgkmcnt(1)
	v_add_f32_e32 v0, v0, v22
	s_waitcnt lgkmcnt(0)
	v_add_f32_e32 v17, v0, v24
	s_waitcnt vmcnt(1)
	v_mov_b32_e32 v0, v200
	v_mov_b32_e32 v1, v201
	v_mov_b32_e32 v2, v202
	v_mov_b32_e32 v3, v203
	v_mov_b32_e32 v4, v204
	v_mov_b32_e32 v5, v205
	v_mov_b32_e32 v6, v206
	v_mov_b32_e32 v7, v207
	v_mov_b32_e32 v8, v208
	v_mov_b32_e32 v9, v209
	v_mov_b32_e32 v10, v210
	v_mov_b32_e32 v11, v211
	v_mov_b32_e32 v12, v212
	v_mov_b32_e32 v13, v213
	v_mov_b32_e32 v14, v214
	v_mov_b32_e32 v15, v215
	v_fma_f32 v37, v16, v17, v12
	v_add_f32_e32 v12, 0, v19
	v_add_f32_e32 v12, v12, v21
	v_add_f32_e32 v12, v12, v23
	v_add_f32_e32 v12, v12, v25
	v_fma_f32 v36, v16, v12, v13
	ds_read2_b32 v[12:13], v135 offset0:2 offset1:3
	v_add_u32_e32 v17, 0x2108, v135
	ds_read2_b32 v[18:19], v17 offset1:1
	v_add_u32_e32 v17, 0x4208, v135
	ds_read2_b32 v[20:21], v17 offset1:1
	v_add_u32_e32 v17, 0x6308, v135
	ds_read2_b32 v[22:23], v17 offset1:1
	s_waitcnt lgkmcnt(3)
; __global__ void __launch_bounds__(512, 2) fwd_kernel(Params p) {
;     ...
;                 float lgv[NE];
; #pragma unroll
;                 for (int e = 0; e < NE; ++e) { float v = 0.f;
; #pragma unroll
;                     for (int q = 0; q < 4; ++q) v += part[((q * 2 + t2) * 32 + jj) * 33 + e];
;                     lgv[e] = v * rstd + p.in[I_BR][e]; }
	v_add_f32_e32 v12, 0, v12
	s_waitcnt lgkmcnt(2)
	v_add_f32_e32 v12, v12, v18
	s_waitcnt lgkmcnt(1)
	v_add_f32_e32 v12, v12, v20
	v_add_u32_e32 v17, 0x2110, v135
	s_waitcnt lgkmcnt(0)
	v_add_f32_e32 v12, v12, v22
	v_fma_f32 v14, v16, v12, v14
	v_add_f32_e32 v12, 0, v13
	v_add_f32_e32 v12, v12, v19
	v_add_f32_e32 v12, v12, v21
	v_add_f32_e32 v12, v12, v23
	v_fmac_f32_e32 v15, v16, v12
	ds_read2_b32 v[12:13], v135 offset0:4 offset1:5
	ds_read2_b32 v[18:19], v17 offset1:1
	v_add_u32_e32 v17, 0x4210, v135
	ds_read2_b32 v[20:21], v17 offset1:1
	v_add_u32_e32 v17, 0x6310, v135
	ds_read2_b32 v[22:23], v17 offset1:1
	s_waitcnt lgkmcnt(3)
	v_add_f32_e32 v12, 0, v12
	s_waitcnt lgkmcnt(2)
	v_add_f32_e32 v12, v12, v18
	s_waitcnt lgkmcnt(1)
	v_add_f32_e32 v12, v12, v20
	v_cmp_lg_f32_e32 vcc, s58, v37
	s_waitcnt lgkmcnt(0)
	v_add_f32_e32 v12, v12, v22
	v_fma_f32 v39, v16, v12, v8
	v_add_f32_e32 v8, 0, v13
	v_add_f32_e32 v8, v8, v19
	v_add_f32_e32 v8, v8, v21
	v_add_f32_e32 v8, v8, v23
	v_fma_f32 v38, v16, v8, v9
	ds_read2_b32 v[8:9], v135 offset0:6 offset1:7
	v_add_u32_e32 v12, 0x2118, v135
	ds_read2_b32 v[12:13], v12 offset1:1
	s_waitcnt lgkmcnt(1)
	v_add_f32_e32 v8, 0, v8
	s_waitcnt lgkmcnt(0)
	v_add_f32_e32 v8, v8, v12
	v_add_u32_e32 v12, 0x4218, v135
	ds_read2_b32 v[18:19], v12 offset1:1
	v_add_u32_e32 v12, 0x6318, v135
	ds_read2_b32 v[20:21], v12 offset1:1
	v_add_u32_e32 v12, 0x2120, v135
	s_waitcnt lgkmcnt(1)
	v_add_f32_e32 v8, v8, v18
	s_waitcnt lgkmcnt(0)
	v_add_f32_e32 v8, v8, v20
	v_fma_f32 v10, v16, v8, v10
	v_add_f32_e32 v8, 0, v9
	v_add_f32_e32 v8, v8, v13
	v_add_f32_e32 v8, v8, v19
	v_add_f32_e32 v8, v8, v21
	v_fmac_f32_e32 v11, v16, v8
	ds_read2_b32 v[8:9], v135 offset0:8 offset1:9
	ds_read2_b32 v[12:13], v12 offset1:1
	s_waitcnt lgkmcnt(1)
	v_add_f32_e32 v8, 0, v8
	s_waitcnt lgkmcnt(0)
	v_add_f32_e32 v8, v8, v12
	v_add_u32_e32 v12, 0x4220, v135
	ds_read2_b32 v[18:19], v12 offset1:1
	v_add_u32_e32 v12, 0x6320, v135
	ds_read2_b32 v[20:21], v12 offset1:1
	s_waitcnt lgkmcnt(1)
	v_add_f32_e32 v8, v8, v18
	s_waitcnt lgkmcnt(0)
	v_add_f32_e32 v8, v8, v20
	v_fma_f32 v41, v16, v8, v4
	v_add_f32_e32 v4, 0, v9
	v_add_f32_e32 v4, v4, v13
	v_add_f32_e32 v4, v4, v19
	v_add_f32_e32 v4, v4, v21
	v_fma_f32 v40, v16, v4, v5
	ds_read2_b32 v[4:5], v135 offset0:10 offset1:11
	v_add_u32_e32 v8, 0x2128, v135
	ds_read2_b32 v[8:9], v8 offset1:1
	s_waitcnt lgkmcnt(1)
	v_add_f32_e32 v4, 0, v4
	s_waitcnt lgkmcnt(0)
	v_add_f32_e32 v4, v4, v8
	v_add_u32_e32 v8, 0x4228, v135
	ds_read2_b32 v[12:13], v8 offset1:1
	v_add_u32_e32 v8, 0x6328, v135
	ds_read2_b32 v[18:19], v8 offset1:1
	v_add_u32_e32 v8, 0x2130, v135
	s_waitcnt lgkmcnt(1)
	v_add_f32_e32 v4, v4, v12
	s_waitcnt lgkmcnt(0)
	v_add_f32_e32 v4, v4, v18
	v_fma_f32 v6, v16, v4, v6
	v_add_f32_e32 v4, 0, v5
	v_add_f32_e32 v4, v4, v9
	v_add_f32_e32 v4, v4, v13
	v_add_f32_e32 v4, v4, v19
	v_fmac_f32_e32 v7, v16, v4
	ds_read2_b32 v[4:5], v135 offset0:12 offset1:13
	ds_read2_b32 v[8:9], v8 offset1:1
	s_waitcnt lgkmcnt(1)
	v_add_f32_e32 v4, 0, v4
	s_waitcnt lgkmcnt(0)
	v_add_f32_e32 v4, v4, v8
	v_add_u32_e32 v8, 0x4230, v135
	ds_read2_b32 v[12:13], v8 offset1:1
	v_add_u32_e32 v8, 0x6330, v135
	ds_read2_b32 v[18:19], v8 offset1:1
	s_waitcnt lgkmcnt(1)
	v_add_f32_e32 v4, v4, v12
	s_waitcnt lgkmcnt(0)
	v_add_f32_e32 v4, v4, v18
	v_fma_f32 v43, v16, v4, v0
	v_add_f32_e32 v0, 0, v5
	v_add_f32_e32 v0, v0, v9
	v_add_f32_e32 v0, v0, v13
	v_add_f32_e32 v0, v0, v19
	v_fma_f32 v42, v16, v0, v1
	ds_read2_b32 v[0:1], v135 offset0:14 offset1:15
	v_add_u32_e32 v4, 0x2138, v135
	ds_read2_b32 v[4:5], v4 offset1:1
	s_waitcnt lgkmcnt(1)
	v_add_f32_e32 v0, 0, v0
	s_waitcnt lgkmcnt(0)
	v_add_f32_e32 v0, v0, v4
	v_add_u32_e32 v4, 0x4238, v135
	ds_read2_b32 v[8:9], v4 offset1:1
	v_add_u32_e32 v4, 0x6338, v135
	ds_read2_b32 v[12:13], v4 offset1:1
	v_add_u32_e32 v4, 0x2140, v135
	s_waitcnt lgkmcnt(1)
	v_add_f32_e32 v0, v0, v8
	s_waitcnt lgkmcnt(0)
	v_add_f32_e32 v0, v0, v12
	v_fma_f32 v2, v16, v0, v2
	v_add_f32_e32 v0, 0, v1
	v_add_f32_e32 v0, v0, v5
	v_add_f32_e32 v0, v0, v9
	v_add_f32_e32 v0, v0, v13
	v_fmac_f32_e32 v3, v16, v0
	ds_read2_b32 v[0:1], v135 offset0:16 offset1:17
	ds_read2_b32 v[4:5], v4 offset1:1
	s_waitcnt lgkmcnt(1)
	v_add_f32_e32 v0, 0, v0
	s_waitcnt lgkmcnt(0)
	v_add_f32_e32 v0, v0, v4
	v_add_u32_e32 v4, 0x4240, v135
	ds_read2_b32 v[8:9], v4 offset1:1
	v_add_u32_e32 v4, 0x6340, v135
	ds_read2_b32 v[12:13], v4 offset1:1
	v_mov_b32_e32 v18, v216
	v_mov_b32_e32 v19, v217
	v_mov_b32_e32 v20, v218
	v_mov_b32_e32 v21, v219
	v_mov_b32_e32 v22, v220
	v_mov_b32_e32 v23, v221
	v_mov_b32_e32 v24, v222
	v_mov_b32_e32 v25, v223
	v_mov_b32_e32 v26, v224
	v_mov_b32_e32 v27, v225
	v_mov_b32_e32 v28, v226
	v_mov_b32_e32 v29, v227
	v_mov_b32_e32 v30, v228
	v_mov_b32_e32 v31, v229
	v_mov_b32_e32 v32, v230
	v_mov_b32_e32 v33, v231
	s_waitcnt lgkmcnt(1)
	v_add_f32_e32 v0, v0, v8
	s_waitcnt lgkmcnt(0)
	v_add_f32_e32 v0, v0, v12
	v_fma_f32 v4, v16, v0, v30
	v_add_f32_e32 v0, 0, v1
	v_add_f32_e32 v0, v0, v5
	v_add_f32_e32 v0, v0, v9
	ds_read2_b32 v[8:9], v135 offset0:18 offset1:19
	v_add_u32_e32 v5, 0x2148, v135
	v_add_f32_e32 v0, v0, v13
	ds_read2_b32 v[12:13], v5 offset1:1
	v_add_u32_e32 v5, 0x4248, v135
	v_fma_f32 v0, v16, v0, v31
	ds_read2_b32 v[30:31], v5 offset1:1
	v_add_u32_e32 v5, 0x6348, v135
	ds_read2_b32 v[44:45], v5 offset1:1
	s_waitcnt lgkmcnt(3)
	v_add_f32_e32 v1, 0, v8
	v_add_f32_e32 v5, 0, v9
	ds_read2_b32 v[8:9], v135 offset0:20 offset1:21
	s_waitcnt lgkmcnt(3)
	v_add_f32_e32 v5, v5, v13
	s_waitcnt lgkmcnt(2)
	v_add_f32_e32 v5, v5, v31
	s_waitcnt lgkmcnt(1)
	v_add_f32_e32 v5, v5, v45
	v_fmac_f32_e32 v33, v16, v5
	s_waitcnt lgkmcnt(0)
; __global__ void __launch_bounds__(512, 2) fwd_kernel(Params p) {
;     ...
;                 float lgv[NE];
; #pragma unroll
;                 for (int e = 0; e < NE; ++e) { float v = 0.f;
; #pragma unroll
;                     for (int q = 0; q < 4; ++q) v += part[((q * 2 + t2) * 32 + jj) * 33 + e];
;                     lgv[e] = v * rstd + p.in[I_BR][e]; }
;                 unsigned mask = 0u; float tv[4];
; #pragma unroll
;                 for (int k = 0; k < 4; ++k) { float best = -__builtin_inff(); int be = 0;
; #pragma unroll
;                     for (int e = 0; e < NE; ++e) { const bool take = !((mask >> e) & 1u) && lgv[e] > best; best = take ? lgv[e] : best; be = take ? e : be; }
	v_add_f32_e32 v5, 0, v8
	v_add_u32_e32 v8, 0x2150, v135
	v_add_f32_e32 v1, v1, v12
	ds_read2_b32 v[12:13], v8 offset1:1
	v_add_u32_e32 v8, 0x4250, v135
	v_add_f32_e32 v1, v1, v30
	ds_read2_b32 v[30:31], v8 offset1:1
	v_add_u32_e32 v8, 0x6350, v135
	v_add_f32_e32 v1, v1, v44
	ds_read2_b32 v[44:45], v8 offset1:1
	s_waitcnt lgkmcnt(2)
	v_add_f32_e32 v5, v5, v12
	s_waitcnt lgkmcnt(1)
	v_add_f32_e32 v5, v5, v30
	v_fma_f32 v1, v16, v1, v32
	s_waitcnt lgkmcnt(0)
	v_add_f32_e32 v5, v5, v44
	v_fma_f32 v8, v16, v5, v26
	v_add_f32_e32 v5, 0, v9
	v_add_f32_e32 v5, v5, v13
	ds_read2_b32 v[12:13], v135 offset0:22 offset1:23
	v_add_f32_e32 v5, v5, v31
	v_add_f32_e32 v5, v5, v45
	v_fma_f32 v5, v16, v5, v27
	s_waitcnt lgkmcnt(0)
	v_add_f32_e32 v9, 0, v12
	v_add_u32_e32 v12, 0x2158, v135
	ds_read2_b32 v[26:27], v12 offset1:1
	v_add_u32_e32 v12, 0x4258, v135
	ds_read2_b32 v[30:31], v12 offset1:1
	v_add_u32_e32 v12, 0x6358, v135
	ds_read2_b32 v[44:45], v12 offset1:1
	v_add_f32_e32 v12, 0, v13
	s_waitcnt lgkmcnt(2)
	v_add_f32_e32 v9, v9, v26
	v_add_f32_e32 v12, v12, v27
	ds_read2_b32 v[26:27], v135 offset0:24 offset1:25
	v_add_u32_e32 v13, 0x2160, v135
	s_waitcnt lgkmcnt(2)
	v_add_f32_e32 v9, v9, v30
	v_add_f32_e32 v12, v12, v31
	ds_read2_b32 v[30:31], v13 offset1:1
	v_add_u32_e32 v13, 0x4260, v135
	s_waitcnt lgkmcnt(2)
	v_add_f32_e32 v9, v9, v44
	v_add_f32_e32 v12, v12, v45
	ds_read2_b32 v[44:45], v13 offset1:1
	v_add_u32_e32 v13, 0x6360, v135
	ds_read2_b32 v[46:47], v13 offset1:1
	v_fmac_f32_e32 v29, v16, v12
	s_waitcnt lgkmcnt(3)
	v_add_f32_e32 v12, 0, v26
	s_waitcnt lgkmcnt(2)
	v_add_f32_e32 v12, v12, v30
	s_waitcnt lgkmcnt(1)
	v_add_f32_e32 v12, v12, v44
	s_waitcnt lgkmcnt(0)
	v_add_f32_e32 v12, v12, v46
	v_fma_f32 v13, v16, v12, v22
	v_add_f32_e32 v12, 0, v27
	v_add_f32_e32 v12, v12, v31
	v_add_f32_e32 v12, v12, v45
	v_add_f32_e32 v12, v12, v47
	v_fma_f32 v12, v16, v12, v23
	ds_read2_b32 v[22:23], v135 offset0:26 offset1:27
	v_fma_f32 v9, v16, v9, v28
	s_waitcnt lgkmcnt(0)
	v_add_f32_e32 v17, 0, v22
	v_add_u32_e32 v22, 0x2168, v135
	ds_read2_b32 v[26:27], v22 offset1:1
	v_add_u32_e32 v22, 0x4268, v135
	ds_read2_b32 v[30:31], v22 offset1:1
	v_add_u32_e32 v22, 0x6368, v135
	ds_read2_b32 v[44:45], v22 offset1:1
	s_waitcnt lgkmcnt(2)
	v_add_f32_e32 v17, v17, v26
	s_waitcnt lgkmcnt(1)
	v_add_f32_e32 v17, v17, v30
	s_waitcnt lgkmcnt(0)
	v_add_f32_e32 v17, v17, v44
	v_fma_f32 v22, v16, v17, v24
	v_add_f32_e32 v17, 0, v23
	v_add_f32_e32 v17, v17, v27
	ds_read2_b32 v[26:27], v135 offset0:28 offset1:29
	v_add_u32_e32 v23, 0x2170, v135
	v_add_f32_e32 v17, v17, v31
	ds_read2_b32 v[30:31], v23 offset1:1
	v_add_u32_e32 v23, 0x4270, v135
	v_add_f32_e32 v17, v17, v45
	ds_read2_b32 v[44:45], v23 offset1:1
	v_add_u32_e32 v23, 0x6370, v135
	ds_read2_b32 v[46:47], v23 offset1:1
	v_fmac_f32_e32 v25, v16, v17
	s_waitcnt lgkmcnt(3)
	v_add_f32_e32 v17, 0, v26
	s_waitcnt lgkmcnt(2)
	v_add_f32_e32 v17, v17, v30
	s_waitcnt lgkmcnt(1)
	v_add_f32_e32 v17, v17, v44
	s_waitcnt lgkmcnt(0)
	v_add_f32_e32 v17, v17, v46
	v_fma_f32 v23, v16, v17, v18
	v_add_f32_e32 v17, 0, v27
	ds_read2_b32 v[26:27], v135 offset0:30 offset1:31
	v_add_u32_e32 v18, 0x2178, v135
	v_add_f32_e32 v17, v17, v31
	ds_read2_b32 v[30:31], v18 offset1:1
	v_add_u32_e32 v18, 0x4278, v135
	v_add_f32_e32 v17, v17, v45
	ds_read2_b32 v[44:45], v18 offset1:1
	v_add_u32_e32 v18, 0x6378, v135
	v_add_f32_e32 v17, v17, v47
	ds_read2_b32 v[46:47], v18 offset1:1
	v_fma_f32 v19, v16, v17, v19
	s_waitcnt lgkmcnt(3)
	v_add_f32_e32 v17, 0, v26
	s_waitcnt lgkmcnt(2)
	v_add_f32_e32 v17, v17, v30
	s_waitcnt lgkmcnt(1)
	v_add_f32_e32 v17, v17, v44
	s_waitcnt lgkmcnt(0)
	v_add_f32_e32 v17, v17, v46
	v_fma_f32 v20, v16, v17, v20
	v_add_f32_e32 v17, 0, v27
	v_add_f32_e32 v17, v17, v31
	v_add_f32_e32 v17, v17, v45
	v_add_f32_e32 v17, v17, v47
	v_fmac_f32_e32 v21, v16, v17
	v_cndmask_b32_e32 v16, v139, v37, vcc
	v_cmp_gt_f32_e32 vcc, v36, v16
	s_nop 1
	v_cndmask_b32_e32 v16, v16, v36, vcc
	v_cndmask_b32_e64 v17, 0, 1, vcc
	v_cmp_gt_f32_e32 vcc, v14, v16
	s_nop 1
	v_cndmask_b32_e32 v16, v16, v14, vcc
	v_cndmask_b32_e64 v17, v17, 2, vcc
	v_cmp_gt_f32_e32 vcc, v15, v16
	s_nop 1
	v_cndmask_b32_e32 v16, v16, v15, vcc
	v_cndmask_b32_e64 v17, v17, 3, vcc
	v_cmp_gt_f32_e32 vcc, v39, v16
	s_nop 1
	v_cndmask_b32_e32 v16, v16, v39, vcc
	v_cndmask_b32_e64 v17, v17, 4, vcc
	v_cmp_gt_f32_e32 vcc, v38, v16
	s_nop 1
	v_cndmask_b32_e32 v16, v16, v38, vcc
	v_cndmask_b32_e64 v17, v17, 5, vcc
	v_cmp_gt_f32_e32 vcc, v10, v16
	s_nop 1
	v_cndmask_b32_e32 v16, v16, v10, vcc
	v_cndmask_b32_e64 v17, v17, 6, vcc
	v_cmp_gt_f32_e32 vcc, v11, v16
	s_nop 1
	v_cndmask_b32_e32 v16, v16, v11, vcc
	v_cndmask_b32_e64 v17, v17, 7, vcc
	v_cmp_gt_f32_e32 vcc, v41, v16
	s_nop 1
	v_cndmask_b32_e32 v16, v16, v41, vcc
	v_cndmask_b32_e64 v17, v17, 8, vcc
	v_cmp_gt_f32_e32 vcc, v40, v16
	s_nop 1
	v_cndmask_b32_e32 v16, v16, v40, vcc
	v_cndmask_b32_e64 v17, v17, 9, vcc
	v_cmp_gt_f32_e32 vcc, v6, v16
	s_nop 1
	v_cndmask_b32_e32 v16, v16, v6, vcc
	v_cndmask_b32_e64 v17, v17, 10, vcc
	v_cmp_gt_f32_e32 vcc, v7, v16
	s_nop 1
	v_cndmask_b32_e32 v16, v16, v7, vcc
	v_cndmask_b32_e64 v17, v17, 11, vcc
	v_cmp_gt_f32_e32 vcc, v43, v16
	s_nop 1
	v_cndmask_b32_e32 v16, v16, v43, vcc
	v_cndmask_b32_e64 v17, v17, 12, vcc
	v_cmp_gt_f32_e32 vcc, v42, v16
	s_nop 1
	v_cndmask_b32_e32 v16, v16, v42, vcc
	v_cndmask_b32_e64 v17, v17, 13, vcc
	v_cmp_gt_f32_e32 vcc, v2, v16
	s_nop 1
	v_cndmask_b32_e32 v16, v16, v2, vcc
	v_cndmask_b32_e64 v17, v17, 14, vcc
	v_cmp_gt_f32_e32 vcc, v3, v16
	s_nop 1
	v_cndmask_b32_e32 v16, v16, v3, vcc
	v_cndmask_b32_e64 v17, v17, 15, vcc
	v_cmp_gt_f32_e32 vcc, v4, v16
	s_nop 1
; __global__ void __launch_bounds__(512, 2) fwd_kernel(Params p) {
;     ...
;                 unsigned mask = 0u; float tv[4];
; #pragma unroll
;                 for (int k = 0; k < 4; ++k) { float best = -__builtin_inff(); int be = 0;
; #pragma unroll
;                     for (int e = 0; e < NE; ++e) { const bool take = !((mask >> e) & 1u) && lgv[e] > best; best = take ? lgv[e] : best; be = take ? e : be; }
;                     mask |= 1u << be; tv[k] = best; te[k] = be; }
	v_cndmask_b32_e32 v16, v16, v4, vcc
	v_cndmask_b32_e64 v17, v17, 16, vcc
	v_cmp_gt_f32_e32 vcc, v0, v16
	s_nop 1
	v_cndmask_b32_e32 v16, v16, v0, vcc
	v_cndmask_b32_e64 v17, v17, 17, vcc
	v_cmp_gt_f32_e32 vcc, v1, v16
	s_nop 1
	v_cndmask_b32_e32 v16, v16, v1, vcc
	v_cndmask_b32_e64 v17, v17, 18, vcc
	v_cmp_gt_f32_e32 vcc, v33, v16
	s_nop 1
	v_cndmask_b32_e32 v16, v16, v33, vcc
	v_cndmask_b32_e64 v17, v17, 19, vcc
	v_cmp_gt_f32_e32 vcc, v8, v16
	s_nop 1
	v_cndmask_b32_e32 v16, v16, v8, vcc
	v_cndmask_b32_e64 v17, v17, 20, vcc
	v_cmp_gt_f32_e32 vcc, v5, v16
	s_nop 1
	v_cndmask_b32_e32 v16, v16, v5, vcc
	v_cndmask_b32_e64 v17, v17, 21, vcc
	v_cmp_gt_f32_e32 vcc, v9, v16
	s_nop 1
	v_cndmask_b32_e32 v16, v16, v9, vcc
	v_cndmask_b32_e64 v17, v17, 22, vcc
	v_cmp_gt_f32_e32 vcc, v29, v16
	s_nop 1
	v_cndmask_b32_e32 v16, v16, v29, vcc
	v_cndmask_b32_e64 v17, v17, 23, vcc
	v_cmp_gt_f32_e32 vcc, v13, v16
	s_nop 1
	v_cndmask_b32_e32 v16, v16, v13, vcc
	v_cndmask_b32_e64 v17, v17, 24, vcc
	v_cmp_gt_f32_e32 vcc, v12, v16
	s_nop 1
	v_cndmask_b32_e32 v16, v16, v12, vcc
	v_cndmask_b32_e64 v17, v17, 25, vcc
	v_cmp_gt_f32_e32 vcc, v22, v16
	s_nop 1
	v_cndmask_b32_e32 v16, v16, v22, vcc
	v_cndmask_b32_e64 v17, v17, 26, vcc
	v_cmp_gt_f32_e32 vcc, v25, v16
	s_nop 1
	v_cndmask_b32_e32 v16, v16, v25, vcc
	v_cndmask_b32_e64 v17, v17, 27, vcc
	v_cmp_gt_f32_e32 vcc, v23, v16
	s_nop 1
	v_cndmask_b32_e32 v16, v16, v23, vcc
	v_cndmask_b32_e64 v17, v17, 28, vcc
	v_cmp_gt_f32_e32 vcc, v19, v16
	s_nop 1
	v_cndmask_b32_e32 v16, v16, v19, vcc
	v_cndmask_b32_e64 v17, v17, 29, vcc
	v_cmp_gt_f32_e32 vcc, v20, v16
	s_nop 1
	v_cndmask_b32_e32 v18, v16, v20, vcc
	v_cndmask_b32_e64 v17, v17, 30, vcc
	v_cmp_gt_f32_e32 vcc, v21, v18
	s_nop 1
	v_cndmask_b32_e64 v16, v17, 31, vcc
	v_cndmask_b32_e32 v24, v18, v21, vcc
	v_cmp_eq_u32_e64 s[10:11], 0, v16
	v_cmp_nlg_f32_e32 vcc, s58, v37
	v_lshlrev_b32_e64 v18, v16, 1
	s_or_b64 s[10:11], s[10:11], vcc
	v_cndmask_b32_e64 v17, v37, v139, s[10:11]
	v_and_b32_e32 v26, 2, v18
	v_cmp_eq_u32_e64 s[10:11], 0, v26
	v_cmp_gt_f32_e64 s[12:13], v36, v17
	s_and_b64 s[10:11], s[10:11], s[12:13]
	v_cndmask_b32_e64 v17, v17, v36, s[10:11]
	v_and_b32_e32 v27, 4, v18
	v_cndmask_b32_e64 v26, 0, 1, s[10:11]
	v_cmp_eq_u32_e64 s[10:11], 0, v27
	v_cmp_gt_f32_e64 s[12:13], v14, v17
	s_and_b64 s[10:11], s[10:11], s[12:13]
	v_cndmask_b32_e64 v17, v17, v14, s[10:11]
	v_and_b32_e32 v27, 8, v18
	v_cndmask_b32_e64 v26, v26, 2, s[10:11]
	v_cmp_eq_u32_e64 s[10:11], 0, v27
	v_cmp_gt_f32_e64 s[12:13], v15, v17
	s_and_b64 s[10:11], s[10:11], s[12:13]
	v_cndmask_b32_e64 v17, v17, v15, s[10:11]
	v_and_b32_e32 v27, 16, v18
	v_cndmask_b32_e64 v26, v26, 3, s[10:11]
	v_cmp_eq_u32_e64 s[10:11], 0, v27
	v_cmp_gt_f32_e64 s[12:13], v39, v17
	s_and_b64 s[10:11], s[10:11], s[12:13]
	v_cndmask_b32_e64 v17, v17, v39, s[10:11]
	v_and_b32_e32 v27, 32, v18
	v_cndmask_b32_e64 v26, v26, 4, s[10:11]
	v_cmp_eq_u32_e64 s[10:11], 0, v27
	v_cmp_gt_f32_e64 s[12:13], v38, v17
	s_and_b64 s[10:11], s[10:11], s[12:13]
	v_cndmask_b32_e64 v17, v17, v38, s[10:11]
	v_and_b32_e32 v27, 64, v18
	v_cndmask_b32_e64 v26, v26, 5, s[10:11]
	v_cmp_eq_u32_e64 s[10:11], 0, v27
	v_cmp_gt_f32_e64 s[12:13], v10, v17
	s_and_b64 s[10:11], s[10:11], s[12:13]
	v_cndmask_b32_e64 v17, v17, v10, s[10:11]
	v_and_b32_e32 v27, 0x80, v18
	v_cndmask_b32_e64 v26, v26, 6, s[10:11]
	v_cmp_eq_u32_e64 s[10:11], 0, v27
	v_cmp_gt_f32_e64 s[12:13], v11, v17
	s_and_b64 s[10:11], s[10:11], s[12:13]
	v_cndmask_b32_e64 v17, v17, v11, s[10:11]
	v_and_b32_e32 v27, 0x100, v18
	v_cndmask_b32_e64 v26, v26, 7, s[10:11]
	v_cmp_eq_u32_e64 s[10:11], 0, v27
	v_cmp_gt_f32_e64 s[12:13], v41, v17
	s_and_b64 s[10:11], s[10:11], s[12:13]
	v_cndmask_b32_e64 v17, v17, v41, s[10:11]
	v_and_b32_e32 v27, 0x200, v18
	v_cndmask_b32_e64 v26, v26, 8, s[10:11]
	v_cmp_eq_u32_e64 s[10:11], 0, v27
	v_cmp_gt_f32_e64 s[12:13], v40, v17
	s_and_b64 s[10:11], s[10:11], s[12:13]
	v_cndmask_b32_e64 v17, v17, v40, s[10:11]
	v_and_b32_e32 v27, 0x400, v18
	v_cndmask_b32_e64 v26, v26, 9, s[10:11]
	v_cmp_eq_u32_e64 s[10:11], 0, v27
	v_cmp_gt_f32_e64 s[12:13], v6, v17
	s_and_b64 s[10:11], s[10:11], s[12:13]
	v_cndmask_b32_e64 v17, v17, v6, s[10:11]
	v_and_b32_e32 v27, 0x800, v18
	v_cndmask_b32_e64 v26, v26, 10, s[10:11]
	v_cmp_eq_u32_e64 s[10:11], 0, v27
	v_cmp_gt_f32_e64 s[12:13], v7, v17
	s_and_b64 s[10:11], s[10:11], s[12:13]
	v_cndmask_b32_e64 v17, v17, v7, s[10:11]
	v_and_b32_e32 v27, 0x1000, v18
	v_cndmask_b32_e64 v26, v26, 11, s[10:11]
	v_cmp_eq_u32_e64 s[10:11], 0, v27
	v_cmp_gt_f32_e64 s[12:13], v43, v17
	s_and_b64 s[10:11], s[10:11], s[12:13]
	v_cndmask_b32_e64 v17, v17, v43, s[10:11]
	v_and_b32_e32 v27, 0x2000, v18
	v_cndmask_b32_e64 v26, v26, 12, s[10:11]
	v_cmp_eq_u32_e64 s[10:11], 0, v27
	v_cmp_gt_f32_e64 s[12:13], v42, v17
	s_and_b64 s[10:11], s[10:11], s[12:13]
	v_cndmask_b32_e64 v17, v17, v42, s[10:11]
	v_and_b32_e32 v27, 0x4000, v18
	v_cndmask_b32_e64 v26, v26, 13, s[10:11]
	v_cmp_eq_u32_e64 s[10:11], 0, v27
	v_cmp_gt_f32_e64 s[12:13], v2, v17
	s_and_b64 s[10:11], s[10:11], s[12:13]
	v_cndmask_b32_e64 v17, v17, v2, s[10:11]
	v_and_b32_e32 v27, 0x8000, v18
	v_cndmask_b32_e64 v26, v26, 14, s[10:11]
	v_cmp_eq_u32_e64 s[10:11], 0, v27
	v_cmp_gt_f32_e64 s[12:13], v3, v17
	s_and_b64 s[10:11], s[10:11], s[12:13]
	v_cndmask_b32_e64 v17, v17, v3, s[10:11]
	v_and_b32_e32 v27, 0x10000, v18
	v_cndmask_b32_e64 v26, v26, 15, s[10:11]
	v_cmp_eq_u32_e64 s[10:11], 0, v27
	v_cmp_gt_f32_e64 s[12:13], v4, v17
	s_and_b64 s[10:11], s[10:11], s[12:13]
	v_cndmask_b32_e64 v17, v17, v4, s[10:11]
	v_and_b32_e32 v27, 0x20000, v18
	v_cndmask_b32_e64 v26, v26, 16, s[10:11]
; __global__ void __launch_bounds__(512, 2) fwd_kernel(Params p) {
;     ...
;                 unsigned mask = 0u; float tv[4];
; #pragma unroll
;                 for (int k = 0; k < 4; ++k) { float best = -__builtin_inff(); int be = 0;
; #pragma unroll
;                     for (int e = 0; e < NE; ++e) { const bool take = !((mask >> e) & 1u) && lgv[e] > best; best = take ? lgv[e] : best; be = take ? e : be; }
;                     mask |= 1u << be; tv[k] = best; te[k] = be; }
	v_cmp_eq_u32_e64 s[10:11], 0, v27
	v_cmp_gt_f32_e64 s[12:13], v0, v17
	s_and_b64 s[10:11], s[10:11], s[12:13]
	v_cndmask_b32_e64 v17, v17, v0, s[10:11]
	v_and_b32_e32 v27, 0x40000, v18
	v_cndmask_b32_e64 v26, v26, 17, s[10:11]
	v_cmp_eq_u32_e64 s[10:11], 0, v27
	v_cmp_gt_f32_e64 s[12:13], v1, v17
	s_and_b64 s[10:11], s[10:11], s[12:13]
	v_cndmask_b32_e64 v17, v17, v1, s[10:11]
	v_and_b32_e32 v27, 0x80000, v18
	v_cndmask_b32_e64 v26, v26, 18, s[10:11]
	v_cmp_eq_u32_e64 s[10:11], 0, v27
	v_cmp_gt_f32_e64 s[12:13], v33, v17
	s_and_b64 s[10:11], s[10:11], s[12:13]
	v_cndmask_b32_e64 v17, v17, v33, s[10:11]
	v_and_b32_e32 v27, 0x100000, v18
	v_cndmask_b32_e64 v26, v26, 19, s[10:11]
	v_cmp_eq_u32_e64 s[10:11], 0, v27
	v_cmp_gt_f32_e64 s[12:13], v8, v17
	s_and_b64 s[10:11], s[10:11], s[12:13]
	v_cndmask_b32_e64 v17, v17, v8, s[10:11]
	v_and_b32_e32 v27, 0x200000, v18
	v_cndmask_b32_e64 v26, v26, 20, s[10:11]
	v_cmp_eq_u32_e64 s[10:11], 0, v27
	v_cmp_gt_f32_e64 s[12:13], v5, v17
	s_and_b64 s[10:11], s[10:11], s[12:13]
	v_cndmask_b32_e64 v17, v17, v5, s[10:11]
	v_and_b32_e32 v27, 0x400000, v18
	v_cndmask_b32_e64 v26, v26, 21, s[10:11]
	v_cmp_eq_u32_e64 s[10:11], 0, v27
	v_cmp_gt_f32_e64 s[12:13], v9, v17
	s_and_b64 s[10:11], s[10:11], s[12:13]
	v_cndmask_b32_e64 v17, v17, v9, s[10:11]
	v_and_b32_e32 v27, 0x800000, v18
	v_cndmask_b32_e64 v26, v26, 22, s[10:11]
	v_cmp_eq_u32_e64 s[10:11], 0, v27
	v_cmp_gt_f32_e64 s[12:13], v29, v17
	s_and_b64 s[10:11], s[10:11], s[12:13]
	v_cndmask_b32_e64 v17, v17, v29, s[10:11]
	v_and_b32_e32 v27, 0x1000000, v18
	v_cndmask_b32_e64 v26, v26, 23, s[10:11]
	v_cmp_eq_u32_e64 s[10:11], 0, v27
	v_cmp_gt_f32_e64 s[12:13], v13, v17
	s_and_b64 s[10:11], s[10:11], s[12:13]
	v_cndmask_b32_e64 v17, v17, v13, s[10:11]
	v_and_b32_e32 v27, 0x2000000, v18
	v_cndmask_b32_e64 v26, v26, 24, s[10:11]
	v_cmp_eq_u32_e64 s[10:11], 0, v27
	v_cmp_gt_f32_e64 s[12:13], v12, v17
	s_and_b64 s[10:11], s[10:11], s[12:13]
	v_cndmask_b32_e64 v17, v17, v12, s[10:11]
	v_and_b32_e32 v27, 0x4000000, v18
	v_cndmask_b32_e64 v26, v26, 25, s[10:11]
	v_cmp_eq_u32_e64 s[10:11], 0, v27
	v_cmp_gt_f32_e64 s[12:13], v22, v17
	s_and_b64 s[10:11], s[10:11], s[12:13]
	v_cndmask_b32_e64 v17, v17, v22, s[10:11]
	v_and_b32_e32 v27, 0x8000000, v18
	v_cndmask_b32_e64 v26, v26, 26, s[10:11]
	v_cmp_eq_u32_e64 s[10:11], 0, v27
	v_cmp_gt_f32_e64 s[12:13], v25, v17
	s_and_b64 s[10:11], s[10:11], s[12:13]
	v_cndmask_b32_e64 v17, v17, v25, s[10:11]
	v_and_b32_e32 v27, 0x10000000, v18
	v_cndmask_b32_e64 v26, v26, 27, s[10:11]
	v_cmp_eq_u32_e64 s[10:11], 0, v27
	v_cmp_gt_f32_e64 s[12:13], v23, v17
	s_and_b64 s[10:11], s[10:11], s[12:13]
	v_cndmask_b32_e64 v17, v17, v23, s[10:11]
	v_and_b32_e32 v27, 0x20000000, v18
	v_cndmask_b32_e64 v26, v26, 28, s[10:11]
	v_cmp_eq_u32_e64 s[10:11], 0, v27
	v_cmp_gt_f32_e64 s[12:13], v19, v17
	s_and_b64 s[10:11], s[10:11], s[12:13]
	v_cndmask_b32_e64 v17, v17, v19, s[10:11]
	v_and_b32_e32 v27, 2.0, v18
	v_cndmask_b32_e64 v26, v26, 29, s[10:11]
	v_cmp_eq_u32_e64 s[10:11], 0, v27
	v_cmp_gt_f32_e64 s[12:13], v20, v17
	s_and_b64 s[10:11], s[10:11], s[12:13]
	v_cndmask_b32_e64 v27, v17, v20, s[10:11]
	v_cndmask_b32_e64 v26, v26, 30, s[10:11]
	v_cmp_ne_u32_e64 s[10:11], 31, v16
	v_cmp_gt_f32_e64 s[12:13], v21, v27
	s_and_b64 s[10:11], s[10:11], s[12:13]
	v_cndmask_b32_e64 v17, v26, 31, s[10:11]
	v_cndmask_b32_e64 v26, v27, v21, s[10:11]
	v_lshl_or_b32 v27, 1, v17, v18
	v_and_b32_e32 v18, 1, v27
	v_cmp_eq_u32_e64 s[10:11], 1, v18
	s_or_b64 s[10:11], s[10:11], vcc
	v_and_b32_e32 v28, 2, v27
	v_cndmask_b32_e64 v18, v37, v139, s[10:11]
	v_cmp_eq_u32_e64 s[10:11], 0, v28
	v_cmp_gt_f32_e64 s[12:13], v36, v18
	s_and_b64 s[10:11], s[10:11], s[12:13]
	v_cndmask_b32_e64 v18, v18, v36, s[10:11]
	v_and_b32_e32 v30, 4, v27
	v_cndmask_b32_e64 v28, 0, 1, s[10:11]
	v_cmp_eq_u32_e64 s[10:11], 0, v30
	v_cmp_gt_f32_e64 s[12:13], v14, v18
	s_and_b64 s[10:11], s[10:11], s[12:13]
	v_cndmask_b32_e64 v18, v18, v14, s[10:11]
	v_and_b32_e32 v30, 8, v27
	v_cndmask_b32_e64 v28, v28, 2, s[10:11]
	v_cmp_eq_u32_e64 s[10:11], 0, v30
	v_cmp_gt_f32_e64 s[12:13], v15, v18
	s_and_b64 s[10:11], s[10:11], s[12:13]
	v_cndmask_b32_e64 v18, v18, v15, s[10:11]
	v_and_b32_e32 v30, 16, v27
	v_cndmask_b32_e64 v28, v28, 3, s[10:11]
	v_cmp_eq_u32_e64 s[10:11], 0, v30
	v_cmp_gt_f32_e64 s[12:13], v39, v18
	s_and_b64 s[10:11], s[10:11], s[12:13]
	v_cndmask_b32_e64 v18, v18, v39, s[10:11]
	v_and_b32_e32 v30, 32, v27
	v_cndmask_b32_e64 v28, v28, 4, s[10:11]
	v_cmp_eq_u32_e64 s[10:11], 0, v30
	v_cmp_gt_f32_e64 s[12:13], v38, v18
	s_and_b64 s[10:11], s[10:11], s[12:13]
	v_cndmask_b32_e64 v18, v18, v38, s[10:11]
	v_and_b32_e32 v30, 64, v27
	v_cndmask_b32_e64 v28, v28, 5, s[10:11]
	v_cmp_eq_u32_e64 s[10:11], 0, v30
	v_cmp_gt_f32_e64 s[12:13], v10, v18
	s_and_b64 s[10:11], s[10:11], s[12:13]
	v_cndmask_b32_e64 v18, v18, v10, s[10:11]
	v_and_b32_e32 v30, 0x80, v27
	v_cndmask_b32_e64 v28, v28, 6, s[10:11]
	v_cmp_eq_u32_e64 s[10:11], 0, v30
	v_cmp_gt_f32_e64 s[12:13], v11, v18
	s_and_b64 s[10:11], s[10:11], s[12:13]
	v_cndmask_b32_e64 v18, v18, v11, s[10:11]
	v_and_b32_e32 v30, 0x100, v27
	v_cndmask_b32_e64 v28, v28, 7, s[10:11]
	v_cmp_eq_u32_e64 s[10:11], 0, v30
	v_cmp_gt_f32_e64 s[12:13], v41, v18
	s_and_b64 s[10:11], s[10:11], s[12:13]
	v_cndmask_b32_e64 v18, v18, v41, s[10:11]
	v_and_b32_e32 v30, 0x200, v27
	v_cndmask_b32_e64 v28, v28, 8, s[10:11]
	v_cmp_eq_u32_e64 s[10:11], 0, v30
	v_cmp_gt_f32_e64 s[12:13], v40, v18
	s_and_b64 s[10:11], s[10:11], s[12:13]
	v_cndmask_b32_e64 v18, v18, v40, s[10:11]
	v_and_b32_e32 v30, 0x400, v27
	v_cndmask_b32_e64 v28, v28, 9, s[10:11]
	v_cmp_eq_u32_e64 s[10:11], 0, v30
; __global__ void __launch_bounds__(512, 2) fwd_kernel(Params p) {
;     ...
;                 unsigned mask = 0u; float tv[4];
; #pragma unroll
;                 for (int k = 0; k < 4; ++k) { float best = -__builtin_inff(); int be = 0;
; #pragma unroll
;                     for (int e = 0; e < NE; ++e) { const bool take = !((mask >> e) & 1u) && lgv[e] > best; best = take ? lgv[e] : best; be = take ? e : be; }
;                     mask |= 1u << be; tv[k] = best; te[k] = be; }
	v_cmp_gt_f32_e64 s[12:13], v6, v18
	s_and_b64 s[10:11], s[10:11], s[12:13]
	v_cndmask_b32_e64 v18, v18, v6, s[10:11]
	v_and_b32_e32 v30, 0x800, v27
	v_cndmask_b32_e64 v28, v28, 10, s[10:11]
	v_cmp_eq_u32_e64 s[10:11], 0, v30
	v_cmp_gt_f32_e64 s[12:13], v7, v18
	s_and_b64 s[10:11], s[10:11], s[12:13]
	v_cndmask_b32_e64 v18, v18, v7, s[10:11]
	v_and_b32_e32 v30, 0x1000, v27
	v_cndmask_b32_e64 v28, v28, 11, s[10:11]
	v_cmp_eq_u32_e64 s[10:11], 0, v30
	v_cmp_gt_f32_e64 s[12:13], v43, v18
	s_and_b64 s[10:11], s[10:11], s[12:13]
	v_cndmask_b32_e64 v18, v18, v43, s[10:11]
	v_and_b32_e32 v30, 0x2000, v27
	v_cndmask_b32_e64 v28, v28, 12, s[10:11]
	v_cmp_eq_u32_e64 s[10:11], 0, v30
	v_cmp_gt_f32_e64 s[12:13], v42, v18
	s_and_b64 s[10:11], s[10:11], s[12:13]
	v_cndmask_b32_e64 v18, v18, v42, s[10:11]
	v_and_b32_e32 v30, 0x4000, v27
	v_cndmask_b32_e64 v28, v28, 13, s[10:11]
	v_cmp_eq_u32_e64 s[10:11], 0, v30
	v_cmp_gt_f32_e64 s[12:13], v2, v18
	s_and_b64 s[10:11], s[10:11], s[12:13]
	v_cndmask_b32_e64 v18, v18, v2, s[10:11]
	v_and_b32_e32 v30, 0x8000, v27
	v_cndmask_b32_e64 v28, v28, 14, s[10:11]
	v_cmp_eq_u32_e64 s[10:11], 0, v30
	v_cmp_gt_f32_e64 s[12:13], v3, v18
	s_and_b64 s[10:11], s[10:11], s[12:13]
	v_cndmask_b32_e64 v18, v18, v3, s[10:11]
	v_and_b32_e32 v30, 0x10000, v27
	v_cndmask_b32_e64 v28, v28, 15, s[10:11]
	v_cmp_eq_u32_e64 s[10:11], 0, v30
	v_cmp_gt_f32_e64 s[12:13], v4, v18
	s_and_b64 s[10:11], s[10:11], s[12:13]
	v_cndmask_b32_e64 v18, v18, v4, s[10:11]
	v_and_b32_e32 v30, 0x20000, v27
	v_cndmask_b32_e64 v28, v28, 16, s[10:11]
	v_cmp_eq_u32_e64 s[10:11], 0, v30
	v_cmp_gt_f32_e64 s[12:13], v0, v18
	s_and_b64 s[10:11], s[10:11], s[12:13]
	v_cndmask_b32_e64 v18, v18, v0, s[10:11]
	v_and_b32_e32 v30, 0x40000, v27
	v_cndmask_b32_e64 v28, v28, 17, s[10:11]
	v_cmp_eq_u32_e64 s[10:11], 0, v30
	v_cmp_gt_f32_e64 s[12:13], v1, v18
	s_and_b64 s[10:11], s[10:11], s[12:13]
	v_cndmask_b32_e64 v18, v18, v1, s[10:11]
	v_and_b32_e32 v30, 0x80000, v27
	v_cndmask_b32_e64 v28, v28, 18, s[10:11]
	v_cmp_eq_u32_e64 s[10:11], 0, v30
	v_cmp_gt_f32_e64 s[12:13], v33, v18
	s_and_b64 s[10:11], s[10:11], s[12:13]
	v_cndmask_b32_e64 v18, v18, v33, s[10:11]
	v_and_b32_e32 v30, 0x100000, v27
	v_cndmask_b32_e64 v28, v28, 19, s[10:11]
	v_cmp_eq_u32_e64 s[10:11], 0, v30
	v_cmp_gt_f32_e64 s[12:13], v8, v18
	s_and_b64 s[10:11], s[10:11], s[12:13]
	v_cndmask_b32_e64 v18, v18, v8, s[10:11]
	v_and_b32_e32 v30, 0x200000, v27
	v_cndmask_b32_e64 v28, v28, 20, s[10:11]
	v_cmp_eq_u32_e64 s[10:11], 0, v30
	v_cmp_gt_f32_e64 s[12:13], v5, v18
	s_and_b64 s[10:11], s[10:11], s[12:13]
	v_cndmask_b32_e64 v18, v18, v5, s[10:11]
	v_and_b32_e32 v30, 0x400000, v27
	v_cndmask_b32_e64 v28, v28, 21, s[10:11]
	v_cmp_eq_u32_e64 s[10:11], 0, v30
	v_cmp_gt_f32_e64 s[12:13], v9, v18
	s_and_b64 s[10:11], s[10:11], s[12:13]
	v_cndmask_b32_e64 v18, v18, v9, s[10:11]
	v_and_b32_e32 v30, 0x800000, v27
	v_cndmask_b32_e64 v28, v28, 22, s[10:11]
	v_cmp_eq_u32_e64 s[10:11], 0, v30
	v_cmp_gt_f32_e64 s[12:13], v29, v18
	s_and_b64 s[10:11], s[10:11], s[12:13]
	v_cndmask_b32_e64 v18, v18, v29, s[10:11]
	v_and_b32_e32 v30, 0x1000000, v27
	v_cndmask_b32_e64 v28, v28, 23, s[10:11]
	v_cmp_eq_u32_e64 s[10:11], 0, v30
	v_cmp_gt_f32_e64 s[12:13], v13, v18
	s_and_b64 s[10:11], s[10:11], s[12:13]
	v_cndmask_b32_e64 v18, v18, v13, s[10:11]
	v_and_b32_e32 v30, 0x2000000, v27
	v_cndmask_b32_e64 v28, v28, 24, s[10:11]
	v_cmp_eq_u32_e64 s[10:11], 0, v30
	v_cmp_gt_f32_e64 s[12:13], v12, v18
	s_and_b64 s[10:11], s[10:11], s[12:13]
	v_cndmask_b32_e64 v18, v18, v12, s[10:11]
	v_and_b32_e32 v30, 0x4000000, v27
	v_cndmask_b32_e64 v28, v28, 25, s[10:11]
	v_cmp_eq_u32_e64 s[10:11], 0, v30
	v_cmp_gt_f32_e64 s[12:13], v22, v18
	s_and_b64 s[10:11], s[10:11], s[12:13]
	v_cndmask_b32_e64 v18, v18, v22, s[10:11]
	v_and_b32_e32 v30, 0x8000000, v27
	v_cndmask_b32_e64 v28, v28, 26, s[10:11]
	v_cmp_eq_u32_e64 s[10:11], 0, v30
	v_cmp_gt_f32_e64 s[12:13], v25, v18
	s_and_b64 s[10:11], s[10:11], s[12:13]
	v_cndmask_b32_e64 v18, v18, v25, s[10:11]
	v_and_b32_e32 v30, 0x10000000, v27
	v_cndmask_b32_e64 v28, v28, 27, s[10:11]
	v_cmp_eq_u32_e64 s[10:11], 0, v30
	v_cmp_gt_f32_e64 s[12:13], v23, v18
	s_and_b64 s[10:11], s[10:11], s[12:13]
	v_cndmask_b32_e64 v18, v18, v23, s[10:11]
	v_and_b32_e32 v30, 0x20000000, v27
	v_cndmask_b32_e64 v28, v28, 28, s[10:11]
	v_cmp_eq_u32_e64 s[10:11], 0, v30
	v_cmp_gt_f32_e64 s[12:13], v19, v18
	s_and_b64 s[10:11], s[10:11], s[12:13]
	v_cndmask_b32_e64 v18, v18, v19, s[10:11]
	v_and_b32_e32 v30, 2.0, v27
	v_cndmask_b32_e64 v28, v28, 29, s[10:11]
	v_cmp_eq_u32_e64 s[10:11], 0, v30
	v_cmp_gt_f32_e64 s[12:13], v20, v18
	s_and_b64 s[10:11], s[10:11], s[12:13]
	v_cndmask_b32_e64 v30, v18, v20, s[10:11]
	v_cndmask_b32_e64 v28, v28, 30, s[10:11]
	v_cmp_lt_i32_e64 s[10:11], -1, v27
	v_cmp_gt_f32_e64 s[12:13], v21, v30
	s_and_b64 s[10:11], s[10:11], s[12:13]
	v_cndmask_b32_e64 v18, v28, 31, s[10:11]
	v_cndmask_b32_e64 v28, v30, v21, s[10:11]
	v_lshlrev_b32_e64 v30, v18, 1
	v_or_b32_e32 v31, v30, v27
	v_and_b32_e32 v32, 1, v31
	v_cmp_eq_u32_e64 s[10:11], 1, v32
	s_or_b64 vcc, s[10:11], vcc
	v_cndmask_b32_e32 v32, v37, v139, vcc
	v_bitop3_b32 v37, v30, 2, v27 bitop3:0xc8
	v_cmp_eq_u32_e32 vcc, 0, v37
	v_cmp_gt_f32_e64 s[10:11], v36, v32
	s_and_b64 vcc, vcc, s[10:11]
	v_cndmask_b32_e32 v32, v32, v36, vcc
	v_bitop3_b32 v36, v30, 4, v27 bitop3:0xc8
	v_cndmask_b32_e64 v37, 0, 1, vcc
	v_cmp_eq_u32_e32 vcc, 0, v36
	v_cmp_gt_f32_e64 s[10:11], v14, v32
	s_and_b64 vcc, vcc, s[10:11]
	v_cndmask_b32_e32 v14, v32, v14, vcc
	v_bitop3_b32 v32, v30, 8, v27 bitop3:0xc8
	v_cndmask_b32_e64 v36, v37, 2, vcc
	v_cmp_eq_u32_e32 vcc, 0, v32
; __global__ void __launch_bounds__(512, 2) fwd_kernel(Params p) {
;     ...
;                 unsigned mask = 0u; float tv[4];
; #pragma unroll
;                 for (int k = 0; k < 4; ++k) { float best = -__builtin_inff(); int be = 0;
; #pragma unroll
;                     for (int e = 0; e < NE; ++e) { const bool take = !((mask >> e) & 1u) && lgv[e] > best; best = take ? lgv[e] : best; be = take ? e : be; }
;                     mask |= 1u << be; tv[k] = best; te[k] = be; }
;                 float ex[4], sum = 0.f;
; #pragma unroll
;                 for (int k = 0; k < 4; ++k) { ex[k] = __expf(tv[k] - tv[0]); sum += ex[k]; }
;                 const float inv = 1.0f / sum;
; #pragma unroll
;                 for (int k = 0; k < 4; ++k) { lrk[tid * 4 + k] = atomicAdd((int*)&hist[te[k]], 1); tok_e[tok * 4 + k] = te[k]; tok_w[tok * 4 + k] = ex[k] * inv; }
	v_cmp_gt_f32_e64 s[10:11], v15, v14
	s_and_b64 vcc, vcc, s[10:11]
	v_cndmask_b32_e32 v14, v14, v15, vcc
	v_bitop3_b32 v15, v30, 16, v27 bitop3:0xc8
	v_cndmask_b32_e64 v32, v36, 3, vcc
	v_cmp_eq_u32_e32 vcc, 0, v15
	v_cmp_gt_f32_e64 s[10:11], v39, v14
	s_and_b64 vcc, vcc, s[10:11]
	v_cndmask_b32_e64 v15, v32, 4, vcc
	v_cndmask_b32_e32 v14, v14, v39, vcc
	v_bitop3_b32 v32, v30, 32, v27 bitop3:0xc8
	v_cmp_eq_u32_e32 vcc, 0, v32
	v_cmp_gt_f32_e64 s[10:11], v38, v14
	s_and_b64 vcc, vcc, s[10:11]
	v_cndmask_b32_e32 v14, v14, v38, vcc
	v_bitop3_b32 v32, v30, 64, v27 bitop3:0xc8
	v_cndmask_b32_e64 v15, v15, 5, vcc
	v_cmp_eq_u32_e32 vcc, 0, v32
	v_cmp_gt_f32_e64 s[10:11], v10, v14
	s_and_b64 vcc, vcc, s[10:11]
	v_cndmask_b32_e32 v10, v14, v10, vcc
	v_bitop3_b32 v14, v30, s0, v27 bitop3:0xc8
	v_cndmask_b32_e64 v15, v15, 6, vcc
	v_cmp_eq_u32_e32 vcc, 0, v14
	v_cmp_gt_f32_e64 s[10:11], v11, v10
	s_and_b64 vcc, vcc, s[10:11]
	s_movk_i32 s0, 0x100
	v_cndmask_b32_e32 v10, v10, v11, vcc
	v_bitop3_b32 v11, v30, s0, v27 bitop3:0xc8
	v_cndmask_b32_e64 v14, v15, 7, vcc
	v_cmp_eq_u32_e32 vcc, 0, v11
	v_cmp_gt_f32_e64 s[10:11], v41, v10
	s_and_b64 vcc, vcc, s[10:11]
	s_movk_i32 s0, 0x200
	v_cndmask_b32_e64 v11, v14, 8, vcc
	v_cndmask_b32_e32 v10, v10, v41, vcc
	v_bitop3_b32 v14, v30, s0, v27 bitop3:0xc8
	v_cmp_eq_u32_e32 vcc, 0, v14
	v_cmp_gt_f32_e64 s[10:11], v40, v10
	s_and_b64 vcc, vcc, s[10:11]
	s_movk_i32 s0, 0x400
	v_cndmask_b32_e32 v10, v10, v40, vcc
	v_bitop3_b32 v14, v30, s0, v27 bitop3:0xc8
	v_cndmask_b32_e64 v11, v11, 9, vcc
	v_cmp_eq_u32_e32 vcc, 0, v14
	v_cmp_gt_f32_e64 s[10:11], v6, v10
	s_and_b64 vcc, vcc, s[10:11]
	v_cndmask_b32_e32 v6, v10, v6, vcc
	v_bitop3_b32 v10, v30, s59, v27 bitop3:0xc8
	v_cndmask_b32_e64 v11, v11, 10, vcc
	v_cmp_eq_u32_e32 vcc, 0, v10
	v_cmp_gt_f32_e64 s[10:11], v7, v6
	s_and_b64 vcc, vcc, s[10:11]
	v_cndmask_b32_e32 v6, v6, v7, vcc
	v_bitop3_b32 v7, v30, s60, v27 bitop3:0xc8
	v_cndmask_b32_e64 v10, v11, 11, vcc
	v_cmp_eq_u32_e32 vcc, 0, v7
	v_cmp_gt_f32_e64 s[10:11], v43, v6
	s_and_b64 vcc, vcc, s[10:11]
	v_cndmask_b32_e64 v7, v10, 12, vcc
	v_cndmask_b32_e32 v6, v6, v43, vcc
	v_bitop3_b32 v10, v30, s61, v27 bitop3:0xc8
	v_cmp_eq_u32_e32 vcc, 0, v10
	v_cmp_gt_f32_e64 s[10:11], v42, v6
	s_and_b64 vcc, vcc, s[10:11]
	s_movk_i32 s0, 0x4000
	v_cndmask_b32_e32 v6, v6, v42, vcc
	v_bitop3_b32 v10, v30, s0, v27 bitop3:0xc8
	v_cndmask_b32_e64 v7, v7, 13, vcc
	v_cmp_eq_u32_e32 vcc, 0, v10
	v_cmp_gt_f32_e64 s[10:11], v2, v6
	s_and_b64 vcc, vcc, s[10:11]
	v_cndmask_b32_e32 v2, v6, v2, vcc
	v_bitop3_b32 v6, v30, s62, v27 bitop3:0xc8
	v_cndmask_b32_e64 v7, v7, 14, vcc
	v_cmp_eq_u32_e32 vcc, 0, v6
	v_cmp_gt_f32_e64 s[10:11], v3, v2
	s_and_b64 vcc, vcc, s[10:11]
	v_cndmask_b32_e32 v2, v2, v3, vcc
	v_bitop3_b32 v3, v30, s63, v27 bitop3:0xc8
	v_cndmask_b32_e64 v6, v7, 15, vcc
	v_cmp_eq_u32_e32 vcc, 0, v3
	v_cmp_gt_f32_e64 s[10:11], v4, v2
	s_and_b64 vcc, vcc, s[10:11]
	v_cndmask_b32_e32 v2, v2, v4, vcc
	v_bitop3_b32 v4, v30, s64, v27 bitop3:0xc8
	v_cndmask_b32_e64 v3, v6, 16, vcc
	v_cmp_eq_u32_e32 vcc, 0, v4
	v_cmp_gt_f32_e64 s[10:11], v0, v2
	s_and_b64 vcc, vcc, s[10:11]
	v_cndmask_b32_e32 v0, v2, v0, vcc
	v_bitop3_b32 v2, v30, s65, v27 bitop3:0xc8
	v_cndmask_b32_e64 v3, v3, 17, vcc
	v_cmp_eq_u32_e32 vcc, 0, v2
	v_cmp_gt_f32_e64 s[10:11], v1, v0
	s_and_b64 vcc, vcc, s[10:11]
	v_cndmask_b32_e32 v0, v0, v1, vcc
	v_bitop3_b32 v1, v30, s66, v27 bitop3:0xc8
	v_cndmask_b32_e64 v2, v3, 18, vcc
	v_cmp_eq_u32_e32 vcc, 0, v1
	v_cmp_gt_f32_e64 s[10:11], v33, v0
	s_and_b64 vcc, vcc, s[10:11]
	v_cndmask_b32_e64 v1, v2, 19, vcc
	v_cndmask_b32_e32 v0, v0, v33, vcc
	v_bitop3_b32 v2, v30, s67, v27 bitop3:0xc8
	v_cmp_eq_u32_e32 vcc, 0, v2
	v_cmp_gt_f32_e64 s[10:11], v8, v0
	s_and_b64 vcc, vcc, s[10:11]
	v_cndmask_b32_e32 v0, v0, v8, vcc
	v_bitop3_b32 v2, v30, s68, v27 bitop3:0xc8
	v_cndmask_b32_e64 v1, v1, 20, vcc
	v_cmp_eq_u32_e32 vcc, 0, v2
	v_cmp_gt_f32_e64 s[10:11], v5, v0
	s_and_b64 vcc, vcc, s[10:11]
	v_cndmask_b32_e32 v0, v0, v5, vcc
	v_bitop3_b32 v2, v30, s69, v27 bitop3:0xc8
	v_cndmask_b32_e64 v1, v1, 21, vcc
	v_cmp_eq_u32_e32 vcc, 0, v2
	v_cmp_gt_f32_e64 s[10:11], v9, v0
	s_and_b64 vcc, vcc, s[10:11]
	v_cndmask_b32_e32 v0, v0, v9, vcc
	v_bitop3_b32 v2, v30, s57, v27 bitop3:0xc8
	v_cndmask_b32_e64 v1, v1, 22, vcc
	v_cmp_eq_u32_e32 vcc, 0, v2
	v_cmp_gt_f32_e64 s[10:11], v29, v0
	s_and_b64 vcc, vcc, s[10:11]
	v_cndmask_b32_e32 v0, v0, v29, vcc
	v_bitop3_b32 v2, v30, s70, v27 bitop3:0xc8
	v_cndmask_b32_e64 v1, v1, 23, vcc
	v_cmp_eq_u32_e32 vcc, 0, v2
	v_cmp_gt_f32_e64 s[10:11], v13, v0
	s_and_b64 vcc, vcc, s[10:11]
	v_cndmask_b32_e32 v0, v0, v13, vcc
	v_bitop3_b32 v2, v30, s71, v27 bitop3:0xc8
	v_cndmask_b32_e64 v1, v1, 24, vcc
	v_cmp_eq_u32_e32 vcc, 0, v2
	v_cmp_gt_f32_e64 s[10:11], v12, v0
	s_and_b64 vcc, vcc, s[10:11]
	v_cndmask_b32_e32 v0, v0, v12, vcc
	v_bitop3_b32 v2, v30, s72, v27 bitop3:0xc8
	v_cndmask_b32_e64 v1, v1, 25, vcc
	v_cmp_eq_u32_e32 vcc, 0, v2
	v_cmp_gt_f32_e64 s[10:11], v22, v0
	s_and_b64 vcc, vcc, s[10:11]
	v_cndmask_b32_e32 v0, v0, v22, vcc
	v_bitop3_b32 v2, v30, s73, v27 bitop3:0xc8
	v_cndmask_b32_e64 v1, v1, 26, vcc
	v_cmp_eq_u32_e32 vcc, 0, v2
	v_cmp_gt_f32_e64 s[10:11], v25, v0
	s_and_b64 vcc, vcc, s[10:11]
	v_cndmask_b32_e32 v0, v0, v25, vcc
	v_bitop3_b32 v2, v30, s74, v27 bitop3:0xc8
	v_cndmask_b32_e64 v1, v1, 27, vcc
	v_cmp_eq_u32_e32 vcc, 0, v2
	v_cmp_gt_f32_e64 s[10:11], v23, v0
	s_and_b64 vcc, vcc, s[10:11]
	v_cndmask_b32_e32 v0, v0, v23, vcc
	v_bitop3_b32 v2, v30, s75, v27 bitop3:0xc8
	v_cndmask_b32_e64 v1, v1, 28, vcc
	v_cmp_eq_u32_e32 vcc, 0, v2
	v_cmp_gt_f32_e64 s[10:11], v19, v0
	s_and_b64 vcc, vcc, s[10:11]
	v_cndmask_b32_e32 v0, v0, v19, vcc
	v_bitop3_b32 v2, v30, 2.0, v27 bitop3:0xc8
	v_cndmask_b32_e64 v1, v1, 29, vcc
	v_cmp_eq_u32_e32 vcc, 0, v2
	v_cmp_gt_f32_e64 s[10:11], v20, v0
	s_and_b64 vcc, vcc, s[10:11]
	v_cndmask_b32_e32 v0, v0, v20, vcc
	v_cndmask_b32_e64 v1, v1, 30, vcc
	v_cmp_lt_i32_e32 vcc, -1, v31
	v_cmp_gt_f32_e64 s[10:11], v21, v0
	s_and_b64 vcc, vcc, s[10:11]
	v_cndmask_b32_e64 v19, v1, 31, vcc
	v_sub_f32_e32 v1, v24, v24
	v_sub_f32_e32 v2, v26, v24
	v_mul_f32_e32 v1, 0x3fb8aa3b, v1
	v_mul_f32_e32 v2, 0x3fb8aa3b, v2
	v_cndmask_b32_e32 v0, v0, v21, vcc
	v_exp_f32_e32 v6, v1
	v_exp_f32_e32 v7, v2
	v_sub_f32_e32 v2, v28, v24
	v_mul_f32_e32 v2, 0x3fb8aa3b, v2
	v_sub_f32_e32 v0, v0, v24
	v_exp_f32_e32 v8, v2
	v_mul_f32_e32 v0, 0x3fb8aa3b, v0
	v_exp_f32_e32 v9, v0
	v_add_f32_e32 v1, 0, v6
	v_add_f32_e32 v1, v1, v7
	v_add_f32_e32 v1, v1, v8
	v_add_f32_e32 v0, v1, v9
	v_div_scale_f32 v1, s[0:1], v0, v0, 1.0
	v_rcp_f32_e32 v2, v1
	v_add_u32_e32 v11, 0, v134
	v_fma_f32 v3, -v1, v2, 1.0
	v_fmac_f32_e32 v2, v3, v2
	v_div_scale_f32 v3, vcc, 1.0, v0, 1.0
	v_mul_f32_e32 v4, v3, v2
	v_fma_f32 v5, -v1, v4, v3
	v_fmac_f32_e32 v4, v5, v2
	v_fma_f32 v1, -v1, v4, v3
	v_div_fmas_f32 v1, v1, v2, v4
	v_div_fixup_f32 v10, v1, v0, 1.0
	v_lshl_add_u32 v1, v16, 2, 0
	ds_add_rtn_u32 v1, v1, v138 offset:53760
	v_lshlrev_b32_e32 v0, 2, v34
	s_waitcnt lgkmcnt(0)
; __global__ void __launch_bounds__(512, 2) fwd_kernel(Params p) {
;     ...
;                 for (int k = 0; k < 4; ++k) { lrk[tid * 4 + k] = atomicAdd((int*)&hist[te[k]], 1); tok_e[tok * 4 + k] = te[k]; tok_w[tok * 4 + k] = ex[k] * inv; }
	ds_write_b32 v11, v1 offset:40960
	v_ashrrev_i32_e32 v1, 31, v0
	v_lshlrev_b64 v[2:3], 2, v[0:1]
	v_lshl_add_u64 v[4:5], s[16:17], 0, v[2:3]
	v_mul_f32_e32 v1, v10, v6
	v_mov_b32_e32 v240, v1
	v_lshl_add_u64 v[2:3], s[42:43], 0, v[2:3]
	global_store_dword v[2:3], v1, off
	v_lshl_add_u32 v1, v17, 2, 0
	ds_add_rtn_u32 v1, v1, v138 offset:53760
	v_or_b32_e32 v2, 1, v0
	v_ashrrev_i32_e32 v3, 31, v2
	v_mul_f32_e32 v0, v10, v7
	v_lshl_add_u64 v[6:7], v[2:3], 2, s[42:43]
	s_waitcnt lgkmcnt(0)
	ds_write_b32 v11, v1 offset:40964
	v_lshl_add_u32 v1, v18, 2, 0
	ds_add_rtn_u32 v1, v1, v138 offset:53760
	v_lshl_add_u32 v2, v19, 2, 0
	s_waitcnt lgkmcnt(0)
	ds_write_b32 v11, v1 offset:40968
	ds_add_rtn_u32 v2, v2, v138 offset:53760
	v_mul_f32_e32 v1, v10, v8
	global_store_dwordx4 v[4:5], v[16:19], off
	s_waitcnt lgkmcnt(0)
	ds_write_b32 v11, v2 offset:40972
	v_mul_f32_e32 v2, v10, v9
	v_mov_b32_e32 v241, v0
	v_mov_b32_e32 v242, v1
	v_mov_b32_e32 v243, v2
	global_store_dwordx3 v[6:7], v[0:2], off
